# baseline (speedup 1.0000x reference)
.LBB0_8:
	v_lshl_or_b32 v96, s55, 8, v92
	v_ashrrev_i32_e32 v97, 31, v96
	v_lshl_add_u64 v[64:65], v[96:97], 2, s[14:15]
	global_load_dwordx4 v[76:79], v[64:65], off
	global_load_dwordx4 v[72:75], v[64:65], off offset:16
	global_load_dwordx4 v[68:71], v[64:65], off offset:512
	s_nop 0
	global_load_dwordx4 v[64:67], v[64:65], off offset:528
	v_lshl_add_u32 v104, s54, 7, v90
	v_mad_i64_i32 v[98:99], s[24:25], v104, s46, 0
	v_or_b32_e32 v100, 16, v104
	v_lshl_add_u64 v[96:97], v[96:97], 1, s[12:13]
	v_or_b32_e32 v102, 32, v104
	v_mad_i64_i32 v[100:101], s[24:25], v100, s46, 0
	v_lshl_add_u64 v[98:99], v[98:99], 1, v[96:97]
	v_mad_i64_i32 v[102:103], s[24:25], v102, s46, 0
	v_lshl_add_u64 v[100:101], v[100:101], 1, v[96:97]
	s_mov_b32 s55, s52
	s_mov_b32 s54, s53
	s_mov_b64 s[26:27], s[22:23]
	s_mov_b64 vcc, s[0:1]
	s_waitcnt vmcnt(0)
	v_add_f32_e32 v62, v62, v78
	v_add_f32_e32 v63, v63, v79
	v_add_f32_e32 v60, v60, v76
	v_add_f32_e32 v61, v61, v77
	v_add_f32_e32 v58, v58, v74
	v_add_f32_e32 v59, v59, v75
	v_add_f32_e32 v56, v56, v72
	v_add_f32_e32 v57, v57, v73
	v_add_f32_e32 v54, v54, v70
	v_add_f32_e32 v55, v55, v71
	v_add_f32_e32 v52, v52, v68
	v_add_f32_e32 v53, v53, v69
	v_add_f32_e32 v50, v50, v66
	v_add_f32_e32 v51, v51, v67
	v_add_f32_e32 v48, v48, v64
	v_add_f32_e32 v49, v49, v65
	v_add_f32_e32 v46, v46, v78
	v_add_f32_e32 v47, v47, v79
	v_add_f32_e32 v44, v44, v76
	v_add_f32_e32 v45, v45, v77
	v_add_f32_e32 v42, v42, v74
	v_add_f32_e32 v43, v43, v75
	v_add_f32_e32 v40, v40, v72
	v_add_f32_e32 v41, v41, v73
	v_add_f32_e32 v38, v38, v70
	v_add_f32_e32 v39, v39, v71
	v_add_f32_e32 v36, v36, v68
	v_add_f32_e32 v37, v37, v69
	v_add_f32_e32 v34, v34, v66
	v_add_f32_e32 v35, v35, v67
	v_add_f32_e32 v32, v32, v64
	v_add_f32_e32 v33, v33, v65
	v_max_f32_e32 v62, 0, v62
	v_max_f32_e32 v58, 0, v58
	v_max_f32_e32 v63, 0, v63
	v_max_f32_e32 v59, 0, v59
	v_max_f32_e32 v60, 0, v60
	v_max_f32_e32 v61, 0, v61
	v_max_f32_e32 v56, 0, v56
	v_max_f32_e32 v57, 0, v57
	v_max_f32_e32 v52, 0, v52
	v_max_f32_e32 v53, 0, v53
	v_max_f32_e32 v48, 0, v48
	v_max_f32_e32 v49, 0, v49
	v_max_f32_e32 v54, 0, v54
	v_max_f32_e32 v55, 0, v55
	v_max_f32_e32 v50, 0, v50
	v_max_f32_e32 v51, 0, v51
	v_max_f32_e32 v44, 0, v44
	v_max_f32_e32 v45, 0, v45
	v_max_f32_e32 v40, 0, v40
	v_max_f32_e32 v105, 0, v41
	v_max_f32_e32 v41, 0, v46
	v_max_f32_e32 v46, 0, v47
	v_max_f32_e32 v42, 0, v42
	v_max_f32_e32 v43, 0, v43
	v_max_f32_e32 v106, 0, v36
	v_max_f32_e32 v107, 0, v37
	v_max_f32_e32 v108, 0, v32
	v_max_f32_e32 v109, 0, v33
	v_max_f32_e32 v110, 0, v38
	v_max_f32_e32 v111, 0, v39
	v_max_f32_e32 v47, 0, v34
	v_max_f32_e32 v112, 0, v35
	v_cvt_pk_f16_f32 v35, v58, v59
	v_cvt_pk_f16_f32 v33, v62, v63
	v_cvt_pk_f16_f32 v34, v56, v57
	v_cvt_pk_f16_f32 v32, v60, v61
	v_add_f32_e32 v30, v30, v78
	v_add_f32_e32 v31, v31, v79
	v_add_f32_e32 v28, v28, v76
	v_add_f32_e32 v29, v29, v77
	v_add_f32_e32 v26, v26, v74
	v_add_f32_e32 v27, v27, v75
	v_add_f32_e32 v24, v24, v72
	v_add_f32_e32 v25, v25, v73
	v_cvt_pk_f16_f32 v39, v50, v51
	v_cvt_pk_f16_f32 v37, v54, v55
	v_cvt_pk_f16_f32 v38, v48, v49
	v_cvt_pk_f16_f32 v36, v52, v53
	v_cvt_pk_f16_f32 v43, v42, v43
	v_cvt_pk_f16_f32 v41, v41, v46
	v_cvt_pk_f16_f32 v42, v40, v105
	v_cvt_pk_f16_f32 v40, v44, v45
	v_cvt_pk_f16_f32 v47, v47, v112
	v_cvt_pk_f16_f32 v45, v110, v111
	v_cvt_pk_f16_f32 v46, v108, v109
	v_cvt_pk_f16_f32 v44, v106, v107
	global_store_dwordx4 v[98:99], v[32:35], off
	global_store_dwordx4 v[98:99], v[36:39], off offset:256
	global_store_dwordx4 v[100:101], v[40:43], off
	global_store_dwordx4 v[100:101], v[44:47], off offset:256
	v_max_f32_e32 v28, 0, v28
	v_max_f32_e32 v24, 0, v24
	v_max_f32_e32 v29, 0, v29
	v_max_f32_e32 v34, 0, v25
	v_max_f32_e32 v25, 0, v30
	v_max_f32_e32 v26, 0, v26
	v_max_f32_e32 v30, 0, v31
	v_max_f32_e32 v27, 0, v27
	v_lshl_add_u64 v[32:33], v[102:103], 1, v[96:97]
	v_cvt_pk_f16_f32 v27, v26, v27
	v_cvt_pk_f16_f32 v25, v25, v30
	v_cvt_pk_f16_f32 v26, v24, v34
	v_cvt_pk_f16_f32 v24, v28, v29
	v_add_f32_e32 v22, v22, v70
	v_add_f32_e32 v23, v23, v71
	v_add_f32_e32 v20, v20, v68
	v_add_f32_e32 v21, v21, v69
	v_add_f32_e32 v18, v18, v66
	v_add_f32_e32 v19, v19, v67
	v_add_f32_e32 v16, v16, v64
	v_add_f32_e32 v17, v17, v65
	global_store_dwordx4 v[32:33], v[24:27], off
	v_max_f32_e32 v20, 0, v20
	v_max_f32_e32 v16, 0, v16
	v_max_f32_e32 v21, 0, v21
	v_max_f32_e32 v24, 0, v17
	v_max_f32_e32 v17, 0, v22
	v_max_f32_e32 v18, 0, v18
	v_max_f32_e32 v22, 0, v23
	v_max_f32_e32 v19, 0, v19
	v_cvt_pk_f16_f32 v19, v18, v19
	v_cvt_pk_f16_f32 v17, v17, v22
	v_cvt_pk_f16_f32 v18, v16, v24
	v_cvt_pk_f16_f32 v16, v20, v21
	global_store_dwordx4 v[32:33], v[16:19], off offset:256
	v_add_f32_e32 v14, v14, v78
	v_add_f32_e32 v15, v15, v79
	v_add_f32_e32 v12, v12, v76
	v_add_f32_e32 v13, v13, v77
	v_or_b32_e32 v16, 48, v104
	v_add_f32_e32 v10, v10, v74
	v_add_f32_e32 v11, v11, v75
	v_add_f32_e32 v8, v8, v72
	v_add_f32_e32 v9, v9, v73
	v_mad_i64_i32 v[16:17], s[24:25], v16, s46, 0
	v_max_f32_e32 v12, 0, v12
	v_max_f32_e32 v8, 0, v8
	v_max_f32_e32 v13, 0, v13
	v_max_f32_e32 v18, 0, v9
	v_max_f32_e32 v9, 0, v14
	v_max_f32_e32 v10, 0, v10
	v_max_f32_e32 v14, 0, v15
	v_max_f32_e32 v11, 0, v11
	v_lshl_add_u64 v[16:17], v[16:17], 1, v[96:97]
	v_cvt_pk_f16_f32 v11, v10, v11
	v_cvt_pk_f16_f32 v9, v9, v14
	v_cvt_pk_f16_f32 v10, v8, v18
	v_cvt_pk_f16_f32 v8, v12, v13
	v_add_f32_e32 v6, v6, v70
	v_add_f32_e32 v7, v7, v71
	v_add_f32_e32 v4, v4, v68
	v_add_f32_e32 v5, v5, v69
	v_add_f32_e32 v2, v2, v66
	v_add_f32_e32 v3, v3, v67
	v_add_f32_e32 v0, v0, v64
	v_add_f32_e32 v1, v1, v65
	global_store_dwordx4 v[16:17], v[8:11], off
	v_max_f32_e32 v4, 0, v4
	v_max_f32_e32 v0, 0, v0
	v_max_f32_e32 v5, 0, v5
	v_max_f32_e32 v8, 0, v1
	v_max_f32_e32 v1, 0, v6
	v_max_f32_e32 v2, 0, v2
	v_max_f32_e32 v6, 0, v7
	v_max_f32_e32 v3, 0, v3
	v_cvt_pk_f16_f32 v3, v2, v3
	v_cvt_pk_f16_f32 v1, v1, v6
	v_cvt_pk_f16_f32 v2, v0, v8
	v_cvt_pk_f16_f32 v0, v4, v5
	s_mov_b64 s[24:25], s[4:5]
	global_store_dwordx4 v[16:17], v[0:3], off offset:256
	s_cbranch_vccnz .LBB0_22

.LBB1_8:
	v_lshl_or_b32 v42, s54, 7, v45
	v_ashrrev_i32_e32 v43, 31, v42
	v_lshl_add_u64 v[56:57], v[42:43], 2, s[14:15]
	global_load_dwordx4 v[48:51], v[56:57], off offset:16
	global_load_dwordx4 v[52:55], v[56:57], off
	v_lshl_add_u32 v56, s53, 7, v44
	v_lshl_add_u64 v[42:43], v[42:43], 1, s[12:13]
	s_mov_b64 vcc, s[0:1]
	s_mov_b32 s54, s51
	s_mov_b32 s53, s52
	s_mov_b64 s[24:25], s[20:21]
	s_waitcnt vmcnt(0)
	v_add_f32_e32 v26, v26, v50
	v_add_f32_e32 v27, v27, v51
	v_add_f32_e32 v28, v28, v52
	v_add_f32_e32 v29, v29, v53
	v_add_f32_e32 v24, v24, v48
	v_add_f32_e32 v25, v25, v49
	v_add_f32_e32 v30, v30, v54
	v_add_f32_e32 v31, v31, v55
	v_max_f32_e32 v28, 0, v28
	v_max_f32_e32 v24, 0, v24
	v_max_f32_e32 v29, 0, v29
	v_max_f32_e32 v57, 0, v25
	v_max_f32_e32 v26, 0, v26
	v_max_f32_e32 v27, 0, v27
	v_max_f32_e32 v25, 0, v30
	v_max_f32_e32 v30, 0, v31
	v_cvt_pk_f16_f32 v27, v26, v27
	v_cvt_pk_f16_f32 v26, v24, v57
	v_cvt_pk_f16_f32 v24, v28, v29
	v_mad_i64_i32 v[28:29], s[22:23], v56, s47, 0
	v_cvt_pk_f16_f32 v25, v25, v30
	v_lshl_add_u64 v[28:29], v[28:29], 1, v[42:43]
	v_add_f32_e32 v20, v20, v52
	v_add_f32_e32 v21, v21, v53
	v_add_f32_e32 v18, v18, v50
	v_add_f32_e32 v19, v19, v51
	v_add_f32_e32 v16, v16, v48
	v_add_f32_e32 v17, v17, v49
	global_store_dwordx4 v[28:29], v[24:27], off
	v_max_f32_e32 v20, 0, v20
	v_max_f32_e32 v16, 0, v16
	v_max_f32_e32 v21, 0, v21
	v_max_f32_e32 v24, 0, v17
	v_max_f32_e32 v18, 0, v18
	v_max_f32_e32 v19, 0, v19
	v_add_f32_e32 v22, v22, v54
	v_add_f32_e32 v23, v23, v55
	v_cvt_pk_f16_f32 v19, v18, v19
	v_cvt_pk_f16_f32 v18, v16, v24
	v_cvt_pk_f16_f32 v16, v20, v21
	v_or_b32_e32 v20, 16, v56
	v_max_f32_e32 v17, 0, v22
	v_max_f32_e32 v22, 0, v23
	v_mad_i64_i32 v[20:21], s[22:23], v20, s47, 0
	v_cvt_pk_f16_f32 v17, v17, v22
	v_lshl_add_u64 v[20:21], v[20:21], 1, v[42:43]
	v_add_f32_e32 v12, v12, v52
	v_add_f32_e32 v13, v13, v53
	v_add_f32_e32 v10, v10, v50
	v_add_f32_e32 v11, v11, v51
	v_add_f32_e32 v8, v8, v48
	v_add_f32_e32 v9, v9, v49
	global_store_dwordx4 v[20:21], v[16:19], off
	v_max_f32_e32 v12, 0, v12
	v_max_f32_e32 v8, 0, v8
	v_max_f32_e32 v13, 0, v13
	v_max_f32_e32 v16, 0, v9
	v_max_f32_e32 v10, 0, v10
	v_max_f32_e32 v11, 0, v11
	v_add_f32_e32 v14, v14, v54
	v_add_f32_e32 v15, v15, v55
	v_cvt_pk_f16_f32 v11, v10, v11
	v_cvt_pk_f16_f32 v10, v8, v16
	v_cvt_pk_f16_f32 v8, v12, v13
	v_or_b32_e32 v12, 32, v56
	v_max_f32_e32 v9, 0, v14
	v_max_f32_e32 v14, 0, v15
	v_mad_i64_i32 v[12:13], s[22:23], v12, s47, 0
	v_cvt_pk_f16_f32 v9, v9, v14
	v_lshl_add_u64 v[12:13], v[12:13], 1, v[42:43]
	v_add_f32_e32 v4, v4, v52
	v_add_f32_e32 v5, v5, v53
	v_add_f32_e32 v2, v2, v50
	v_add_f32_e32 v3, v3, v51
	v_add_f32_e32 v0, v0, v48
	v_add_f32_e32 v1, v1, v49
	global_store_dwordx4 v[12:13], v[8:11], off
	v_max_f32_e32 v4, 0, v4
	v_max_f32_e32 v0, 0, v0
	v_max_f32_e32 v5, 0, v5
	v_max_f32_e32 v8, 0, v1
	v_max_f32_e32 v2, 0, v2
	v_max_f32_e32 v3, 0, v3
	v_add_f32_e32 v6, v6, v54
	v_add_f32_e32 v7, v7, v55
	v_cvt_pk_f16_f32 v3, v2, v3
	v_cvt_pk_f16_f32 v2, v0, v8
	v_cvt_pk_f16_f32 v0, v4, v5
	v_or_b32_e32 v4, 48, v56
	v_max_f32_e32 v1, 0, v6
	v_max_f32_e32 v6, 0, v7
	v_mad_i64_i32 v[4:5], s[22:23], v4, s47, 0
	v_cvt_pk_f16_f32 v1, v1, v6
	v_lshl_add_u64 v[4:5], v[4:5], 1, v[42:43]
	s_mov_b64 s[22:23], s[4:5]
	global_store_dwordx4 v[4:5], v[0:3], off
	s_cbranch_vccnz .LBB1_22

_Z10rnn_kernelPKDF16_S0_PDF16_S1_:
	s_load_dwordx8 s[4:11], s[0:1], 0x0
	v_readfirstlane_b32 s0, v0
	s_lshr_b32 s12, s0, 6
	s_lshl_b32 s0, s12, 4
	s_mov_b32 s1, 0
	s_lshl_b64 s[14:15], s[0:1], 13
	v_and_b32_e32 v1, 63, v0
	s_waitcnt lgkmcnt(0)
	s_add_u32 s6, s6, s14
	s_addc_u32 s7, s7, s15
	v_lshlrev_b32_e32 v142, 4, v1
	v_mov_b32_e32 v143, 0
	v_lshl_add_u64 v[2:3], s[6:7], 0, v[142:143]
	s_movk_i32 s3, 0x1000
	v_add_co_u32_e32 v4, vcc, s3, v2
	s_mov_b32 s13, 0x18000
	s_nop 0
	v_addc_co_u32_e32 v5, vcc, 0, v3, vcc
	v_add_co_u32_e32 v110, vcc, s13, v2
	s_mov_b32 s13, 0x19000
	s_nop 0
	v_addc_co_u32_e32 v111, vcc, 0, v3, vcc
	v_add_co_u32_e32 v50, vcc, s13, v2
	s_mov_b32 s13, 0x1a000
	s_nop 0
	v_addc_co_u32_e32 v51, vcc, 0, v3, vcc
	v_add_co_u32_e32 v52, vcc, s13, v2
	s_movk_i32 s3, 0x2000
	s_nop 0
	v_addc_co_u32_e32 v53, vcc, 0, v3, vcc
	v_add_co_u32_e32 v54, vcc, s3, v2
	s_movk_i32 s3, 0x3000
	s_nop 0
	v_addc_co_u32_e32 v55, vcc, 0, v3, vcc
	global_load_dwordx4 v[6:9], v[110:111], off
	global_load_dwordx4 v[10:13], v[110:111], off offset:1024
	global_load_dwordx4 v[14:17], v[110:111], off offset:2048
	global_load_dwordx4 v[18:21], v[110:111], off offset:3072
	global_load_dwordx4 v[22:25], v[50:51], off offset:1024
	global_load_dwordx4 v[26:29], v[50:51], off offset:2048
	global_load_dwordx4 a[0:3], v[4:5], off offset:1024
	global_load_dwordx4 a[4:7], v[4:5], off offset:2048
	global_load_dwordx4 a[8:11], v[54:55], off offset:-4096
	global_load_dwordx4 a[12:15], v[54:55], off
	global_load_dwordx4 a[16:19], v[54:55], off offset:1024
	global_load_dwordx4 a[20:23], v[54:55], off offset:2048
	global_load_dwordx4 v[30:33], v[50:51], off offset:3072
	global_load_dwordx4 v[34:37], v[52:53], off offset:-4096
	global_load_dwordx4 v[38:41], v[52:53], off
	global_load_dwordx4 v[42:45], v[52:53], off offset:1024
	global_load_dwordx4 v[46:49], v[52:53], off offset:2048
	v_add_co_u32_e32 v50, vcc, s3, v2
	s_movk_i32 s3, 0x4000
	s_nop 0
	v_addc_co_u32_e32 v51, vcc, 0, v3, vcc
	v_add_co_u32_e32 v56, vcc, s3, v2
	s_movk_i32 s3, 0x5000
	s_nop 0
	v_addc_co_u32_e32 v57, vcc, 0, v3, vcc
	global_load_dwordx4 a[24:27], v[54:55], off offset:3072
	global_load_dwordx4 a[28:31], v[56:57], off offset:-4096
	global_load_dwordx4 a[32:35], v[4:5], off offset:3072
	global_load_dwordx4 a[36:39], v[50:51], off offset:1024
	global_load_dwordx4 a[40:43], v[50:51], off offset:2048
	global_load_dwordx4 a[44:47], v[50:51], off offset:3072
	global_load_dwordx4 a[48:51], v[56:57], off
	global_load_dwordx4 a[52:55], v[56:57], off offset:1024
	global_load_dwordx4 a[56:59], v[56:57], off offset:2048
	global_load_dwordx4 a[60:63], v[56:57], off offset:3072
	v_add_co_u32_e32 v4, vcc, s3, v2
	s_movk_i32 s3, 0x6000
	s_nop 0
	v_addc_co_u32_e32 v5, vcc, 0, v3, vcc
	v_add_co_u32_e32 v98, vcc, s3, v2
	s_movk_i32 s3, 0x7000
	s_nop 0
	v_addc_co_u32_e32 v99, vcc, 0, v3, vcc
	v_add_co_u32_e32 v100, vcc, s3, v2
	s_mov_b32 s3, 0x8000
	s_nop 0
	v_addc_co_u32_e32 v101, vcc, 0, v3, vcc
	global_load_dwordx4 v[50:53], v[52:53], off offset:3072
	v_add_co_u32_e32 v102, vcc, s3, v2
	s_mov_b32 s14, 0x1c000
	s_nop 0
	v_addc_co_u32_e32 v103, vcc, 0, v3, vcc
	v_add_co_u32_e32 v82, vcc, s14, v2
	global_load_dwordx4 a[64:67], v[4:5], off offset:1024
	global_load_dwordx4 a[68:71], v[4:5], off offset:2048
	global_load_dwordx4 a[72:75], v[98:99], off offset:-4096
	global_load_dwordx4 a[76:79], v[98:99], off
	global_load_dwordx4 a[80:83], v[98:99], off offset:1024
	global_load_dwordx4 a[84:87], v[98:99], off offset:2048
	v_addc_co_u32_e32 v83, vcc, 0, v3, vcc
	global_load_dwordx4 v[54:57], v[82:83], off offset:-4096
	s_mov_b32 s13, 0x1b000
	v_add_co_u32_e32 v66, vcc, s13, v2
	s_mov_b32 s13, 0x1d000
	s_nop 0
	v_addc_co_u32_e32 v67, vcc, 0, v3, vcc
	global_load_dwordx4 v[58:61], v[66:67], off offset:1024
	global_load_dwordx4 v[62:65], v[66:67], off offset:2048
	s_nop 0
	global_load_dwordx4 v[66:69], v[66:67], off offset:3072
	s_nop 0
	global_load_dwordx4 v[70:73], v[82:83], off
	global_load_dwordx4 v[74:77], v[82:83], off offset:1024
	global_load_dwordx4 v[78:81], v[82:83], off offset:2048
	s_nop 0
	global_load_dwordx4 v[82:85], v[82:83], off offset:3072
	v_add_co_u32_e32 v104, vcc, s13, v2
	s_mov_b32 s13, 0x1e000
	s_nop 0
	v_addc_co_u32_e32 v105, vcc, 0, v3, vcc
	v_add_co_u32_e32 v106, vcc, s13, v2
	s_lshl_b32 s13, s12, 15
	s_nop 0
	v_addc_co_u32_e32 v107, vcc, 0, v3, vcc
	global_load_dwordx4 v[86:89], v[106:107], off offset:-4096
	global_load_dwordx4 v[90:93], v[104:105], off offset:1024
	global_load_dwordx4 v[94:97], v[104:105], off offset:2048
	global_load_dwordx4 a[88:91], v[98:99], off offset:3072
	global_load_dwordx4 a[92:95], v[102:103], off offset:-4096
	global_load_dwordx4 a[96:99], v[4:5], off offset:3072
	global_load_dwordx4 a[100:103], v[100:101], off offset:1024
	global_load_dwordx4 a[104:107], v[100:101], off offset:2048
	global_load_dwordx4 a[108:111], v[100:101], off offset:3072
	global_load_dwordx4 a[112:115], v[102:103], off
	global_load_dwordx4 a[116:119], v[102:103], off offset:1024
	global_load_dwordx4 a[120:123], v[102:103], off offset:2048
	global_load_dwordx4 a[124:127], v[102:103], off offset:3072
	s_add_i32 s13, s13, 0
	v_add_u32_e32 v213, s13, v142
	s_mov_b32 s13, 0x9000
	s_waitcnt vmcnt(54)
	ds_write_b128 v213, v[6:9]
	s_waitcnt vmcnt(53)
	ds_write_b128 v213, v[10:13] offset:1024
	s_waitcnt vmcnt(52)
	ds_write_b128 v213, v[14:17] offset:2048
	s_waitcnt vmcnt(51)
	ds_write_b128 v213, v[18:21] offset:3072
	s_waitcnt vmcnt(41)
	ds_write_b128 v213, v[34:37] offset:4096
	ds_write_b128 v213, v[22:25] offset:5120
	ds_write_b128 v213, v[26:29] offset:6144
	ds_write_b128 v213, v[30:33] offset:7168
	s_waitcnt vmcnt(40)
	ds_write_b128 v213, v[38:41] offset:8192
	s_waitcnt vmcnt(39)
	ds_write_b128 v213, v[42:45] offset:9216
	s_waitcnt vmcnt(38)
	ds_write_b128 v213, v[46:49] offset:10240
	v_add_co_u32_e32 v8, vcc, s13, v2
	s_mov_b32 s13, 0xa000
	s_nop 0
	v_addc_co_u32_e32 v9, vcc, 0, v3, vcc
	v_add_co_u32_e32 v10, vcc, s13, v2
	s_mov_b32 s13, 0xb000
	s_nop 0
	v_addc_co_u32_e32 v11, vcc, 0, v3, vcc
	v_add_co_u32_e32 v12, vcc, s13, v2
	s_mov_b32 s13, 0xc000
	s_nop 0
	v_addc_co_u32_e32 v13, vcc, 0, v3, vcc
	v_and_b32_e32 v32, 15, v0
	v_lshl_or_b32 v206, s2, 4, v32
	v_ashrrev_i32_e32 v207, 31, v206
	v_bfe_u32 v1, v0, 5, 1
	v_lshlrev_b64 v[144:145], 10, v[206:207]
	v_or_b32_e32 v33, s0, v1
	v_bitop3_b32 v1, v1, v32, s0 bitop3:0x36
	s_lshl_b32 s0, s12, 8
	s_mov_b32 s2, 0x400000
	v_bitop3_b32 v153, v33, v32, 12 bitop3:0x36
	v_bitop3_b32 v154, v33, v32, 14 bitop3:0x36
	s_waitcnt vmcnt(27)
	ds_write_b128 v213, v[50:53] offset:11264
	global_load_dwordx4 a[128:131], v[8:9], off offset:1024
	global_load_dwordx4 a[132:135], v[8:9], off offset:2048
	global_load_dwordx4 a[136:139], v[10:11], off offset:-4096
	global_load_dwordx4 a[140:143], v[10:11], off
	global_load_dwordx4 v[4:7], v[104:105], off offset:3072
	global_load_dwordx4 a[144:147], v[10:11], off offset:1024
	global_load_dwordx4 a[148:151], v[10:11], off offset:2048
	global_load_dwordx4 a[152:155], v[8:9], off offset:3072
	global_load_dwordx4 a[156:159], v[12:13], off offset:1024
	global_load_dwordx4 a[160:163], v[12:13], off offset:2048
	global_load_dwordx4 a[164:167], v[12:13], off offset:3072
	v_add_co_u32_e32 v12, vcc, s13, v2
	v_bfe_u32 v218, v0, 4, 2
	s_nop 0
	v_addc_co_u32_e32 v13, vcc, 0, v3, vcc
	global_load_dwordx4 a[168:171], v[10:11], off offset:3072
	global_load_dwordx4 a[172:175], v[12:13], off offset:-4096
	s_waitcnt vmcnt(33)
	ds_write_b128 v213, v[54:57] offset:12288
	global_load_dwordx4 v[8:11], v[106:107], off
	global_load_dwordx4 a[176:179], v[12:13], off
	global_load_dwordx4 a[180:183], v[12:13], off offset:1024
	global_load_dwordx4 a[184:187], v[12:13], off offset:2048
	global_load_dwordx4 a[188:191], v[12:13], off offset:3072
	s_waitcnt vmcnt(37)
	ds_write_b128 v213, v[58:61] offset:13312
	global_load_dwordx4 v[12:15], v[106:107], off offset:1024
	global_load_dwordx4 a[192:195], v142, s[6:7]
	global_load_dwordx4 a[196:199], v142, s[6:7] offset:1024
	global_load_dwordx4 a[200:203], v142, s[6:7] offset:2048
	global_load_dwordx4 a[204:207], v142, s[6:7] offset:3072
	s_mov_b32 s7, 0x1f000
	v_add_co_u32_e32 v16, vcc, s7, v2
	s_waitcnt vmcnt(41)
	ds_write_b128 v213, v[62:65] offset:14336
	global_load_dwordx4 v[24:27], v[106:107], off offset:2048
	s_waitcnt vmcnt(41)
	ds_write_b128 v213, v[66:69] offset:15360
	s_waitcnt vmcnt(40)
	ds_write_b128 v213, v[70:73] offset:16384
	s_waitcnt vmcnt(39)
	ds_write_b128 v213, v[74:77] offset:17408
	s_waitcnt vmcnt(38)
	ds_write_b128 v213, v[78:81] offset:18432
	s_waitcnt vmcnt(37)
	ds_write_b128 v213, v[82:85] offset:19456
	s_waitcnt vmcnt(36)
	ds_write_b128 v213, v[86:89] offset:20480
	s_waitcnt vmcnt(35)
	ds_write_b128 v213, v[90:93] offset:21504
	s_waitcnt vmcnt(34)
	ds_write_b128 v213, v[94:97] offset:22528
	v_addc_co_u32_e32 v17, vcc, 0, v3, vcc
	global_load_dwordx4 v[28:31], v[106:107], off offset:3072
	global_load_dwordx4 v[36:39], v[16:17], off
	global_load_dwordx4 v[40:43], v[16:17], off offset:1024
	global_load_dwordx4 v[48:51], v[16:17], off offset:2048
	global_load_dwordx4 v[52:55], v[16:17], off offset:3072
	v_lshl_add_u64 v[16:17], s[4:5], 0, v[144:145]
	v_lshl_add_u64 v[16:17], v[16:17], 0, s[0:1]
	v_and_b32_e32 v142, 48, v0
	v_lshl_add_u64 v[18:19], v[16:17], 0, v[142:143]
	global_load_dwordx4 v[56:59], v[18:19], off
	s_mov_b32 s1, 0xe000
	v_add_co_u32_e32 v16, vcc, s1, v2
	s_mov_b32 s6, 0xd000
	s_nop 0
	v_addc_co_u32_e32 v17, vcc, 0, v3, vcc
	v_add_co_u32_e32 v20, vcc, s6, v2
	s_mov_b32 s1, 0xf000
	s_nop 0
	v_addc_co_u32_e32 v21, vcc, 0, v3, vcc
	global_load_dwordx4 a[208:211], v[16:17], off offset:-4096
	global_load_dwordx4 a[212:215], v[16:17], off
	global_load_dwordx4 a[216:219], v[16:17], off offset:1024
	global_load_dwordx4 a[220:223], v[16:17], off offset:2048
	global_load_dwordx4 a[224:227], v[20:21], off offset:1024
	global_load_dwordx4 a[228:231], v[20:21], off offset:2048
	v_lshlrev_b32_e32 v143, 10, v32
	v_or_b32_e32 v144, v144, v142
	s_waitcnt vmcnt(31)
	ds_write_b128 v213, v[4:7] offset:23552
	v_add_co_u32_e32 v6, vcc, s1, v2
	s_mov_b32 s1, 0x10000
	s_nop 0
	v_addc_co_u32_e32 v7, vcc, 0, v3, vcc
	v_add_co_u32_e32 v22, vcc, s1, v2
	s_mov_b32 s1, 0x11000
	s_nop 0
	v_addc_co_u32_e32 v23, vcc, 0, v3, vcc
	global_load_dwordx4 a[232:235], v[16:17], off offset:3072
	global_load_dwordx4 a[236:239], v[22:23], off offset:-4096
	global_load_dwordx4 a[240:243], v[20:21], off offset:3072
	global_load_dwordx4 a[244:247], v[6:7], off offset:1024
	s_waitcnt vmcnt(26)
	ds_write_b128 v213, v[8:11] offset:24576
	s_waitcnt vmcnt(21)
	ds_write_b128 v213, v[12:15] offset:25600
	global_load_dwordx4 v[10:13], v[18:19], off offset:64
	v_add_co_u32_e32 v34, vcc, s1, v2
	s_mov_b32 s1, 0x12000
	s_nop 0
	v_addc_co_u32_e32 v35, vcc, 0, v3, vcc
	v_add_co_u32_e32 v66, vcc, s1, v2
	s_mov_b32 s1, 0x13000
	s_nop 0
	v_addc_co_u32_e32 v67, vcc, 0, v3, vcc
	v_add_co_u32_e32 v46, vcc, s1, v2
	s_mov_b32 s1, 0x14000
	s_nop 0
	v_addc_co_u32_e32 v47, vcc, 0, v3, vcc
	v_add_co_u32_e32 v86, vcc, s1, v2
	s_mov_b32 s1, 0x15000
	s_nop 0
	v_addc_co_u32_e32 v87, vcc, 0, v3, vcc
	v_add_co_u32_e32 v122, vcc, s1, v2
	s_mov_b32 s1, 0x16000
	s_nop 0
	v_addc_co_u32_e32 v123, vcc, 0, v3, vcc
	v_lshrrev_b32_e32 v14, 1, v0
	v_add_co_u32_e32 v106, vcc, s1, v2
	v_and_or_b32 v152, v14, 8, v143
	s_waitcnt vmcnt(11)
	v_cvt_f32_f16_e32 v14, v56
	v_addc_co_u32_e32 v107, vcc, 0, v3, vcc
	s_mov_b32 s1, 0x17000
	ds_write_b128 v213, v[24:27] offset:26624
	ds_write_b128 v213, v[28:31] offset:27648
	v_add_co_u32_e32 v134, vcc, s1, v2
	ds_write_b128 v213, v[36:39] offset:28672
	s_nop 0
	v_addc_co_u32_e32 v135, vcc, 0, v3, vcc
	global_load_dwordx4 v[2:5], v[6:7], off offset:2048
	s_nop 0
	global_load_dwordx4 v[6:9], v[6:7], off offset:3072
	ds_write_b128 v213, v[40:43] offset:29696
	ds_write_b128 v213, v[48:51] offset:30720
	ds_write_b128 v213, v[52:55] offset:31744
	v_lshl_add_u32 v217, v1, 4, v152
	v_bitop3_b32 v1, v33, v32, 2 bitop3:0x36
	v_lshl_add_u32 v215, v1, 4, v152
	v_exp_f32_e32 v1, v14
	global_load_dwordx4 v[14:17], v[18:19], off offset:128
	global_load_dwordx4 v[138:141], v[18:19], off offset:192
	v_cvt_f32_f16_sdwa v20, v56 dst_sel:DWORD dst_unused:UNUSED_PAD src0_sel:WORD_1
	v_cvt_f32_f16_e32 v21, v57
	v_cvt_f32_f16_sdwa v25, v57 dst_sel:DWORD dst_unused:UNUSED_PAD src0_sel:WORD_1
	v_add_f32_e32 v1, 1.0, v1
	v_exp_f32_e32 v24, v20
	v_rcp_f32_e32 v20, v1
	v_exp_f32_e32 v1, v21
	v_exp_f32_e32 v25, v25
	v_add_f32_e32 v21, 1.0, v24
	v_rcp_f32_e32 v21, v21
	v_add_f32_e32 v1, 1.0, v1
	v_rcp_f32_e32 v24, v1
	v_add_f32_e32 v1, 1.0, v25
	v_rcp_f32_e32 v25, v1
	v_fma_f32 v20, v20, -2.0, 1.0
	v_fma_f32 v21, v21, -2.0, 1.0
	v_cvt_f32_f16_e32 v1, v58
	s_add_i32 s1, 0, 0x24000
	v_fma_f32 v24, v24, -2.0, 1.0
	v_fma_f32 v25, v25, -2.0, 1.0
	v_cvt_pk_f16_f32 v20, v20, v21
	v_cvt_pk_f16_f32 v21, v24, v25
	v_add_u32_e32 v24, s1, v217
	ds_write_b64 v24, v[20:21]
	v_cvt_f32_f16_sdwa v20, v58 dst_sel:DWORD dst_unused:UNUSED_PAD src0_sel:WORD_1
	v_exp_f32_e32 v1, v1
	v_cvt_f32_f16_e32 v21, v59
	v_cvt_f32_f16_sdwa v24, v59 dst_sel:DWORD dst_unused:UNUSED_PAD src0_sel:WORD_1
	v_exp_f32_e32 v25, v20
	v_add_f32_e32 v1, 1.0, v1
	v_rcp_f32_e32 v20, v1
	v_exp_f32_e32 v1, v21
	v_add_f32_e32 v21, 1.0, v25
	v_exp_f32_e32 v25, v24
	v_rcp_f32_e32 v21, v21
	v_add_f32_e32 v1, 1.0, v1
	v_rcp_f32_e32 v24, v1
	v_add_f32_e32 v1, 1.0, v25
	v_rcp_f32_e32 v25, v1
	s_waitcnt vmcnt(4)
	v_cvt_f32_f16_e32 v1, v10
	v_cvt_f32_f16_sdwa v10, v10 dst_sel:DWORD dst_unused:UNUSED_PAD src0_sel:WORD_1
	v_fma_f32 v20, v20, -2.0, 1.0
	v_fma_f32 v21, v21, -2.0, 1.0
	v_fma_f32 v24, v24, -2.0, 1.0
	v_fma_f32 v25, v25, -2.0, 1.0
	v_cvt_pk_f16_f32 v20, v20, v21
	v_cvt_pk_f16_f32 v21, v24, v25
	v_exp_f32_e32 v1, v1
	v_add_u32_e32 v24, s1, v215
	ds_write_b64 v24, v[20:21]
	v_cvt_f32_f16_e32 v20, v11
	v_exp_f32_e32 v21, v10
	v_cvt_f32_f16_sdwa v11, v11 dst_sel:DWORD dst_unused:UNUSED_PAD src0_sel:WORD_1
	v_add_f32_e32 v1, 1.0, v1
	v_rcp_f32_e32 v10, v1
	v_exp_f32_e32 v1, v20
	v_add_f32_e32 v20, 1.0, v21
	v_exp_f32_e32 v21, v11
	v_rcp_f32_e32 v11, v20
	v_add_f32_e32 v1, 1.0, v1
	v_rcp_f32_e32 v20, v1
	v_add_f32_e32 v1, 1.0, v21
	v_rcp_f32_e32 v21, v1
	v_bitop3_b32 v26, v33, v32, 4 bitop3:0x36
	v_bitop3_b32 v1, v33, v32, 6 bitop3:0x36
	v_lshl_add_u32 v211, v26, 4, v152
	v_lshl_add_u32 v212, v1, 4, v152
	v_fma_f32 v10, v10, -2.0, 1.0
	v_fma_f32 v11, v11, -2.0, 1.0
	v_fma_f32 v20, v20, -2.0, 1.0
	v_fma_f32 v21, v21, -2.0, 1.0
	v_bitop3_b32 v1, v33, v32, 8 bitop3:0x36
	v_cvt_pk_f16_f32 v10, v10, v11
	v_cvt_pk_f16_f32 v11, v20, v21
	v_lshl_add_u32 v210, v1, 4, v152
	v_add_u32_e32 v1, s1, v211
	ds_write_b64 v1, v[10:11]
	v_cvt_f32_f16_e32 v10, v12
	v_cvt_f32_f16_sdwa v11, v12 dst_sel:DWORD dst_unused:UNUSED_PAD src0_sel:WORD_1
	v_cvt_f32_f16_e32 v12, v13
	v_cvt_f32_f16_sdwa v13, v13 dst_sel:DWORD dst_unused:UNUSED_PAD src0_sel:WORD_1
	v_exp_f32_e32 v10, v10
	v_exp_f32_e32 v11, v11
	v_exp_f32_e32 v12, v12
	v_exp_f32_e32 v13, v13
	v_add_f32_e32 v10, 1.0, v10
	v_add_f32_e32 v11, 1.0, v11
	v_add_f32_e32 v12, 1.0, v12
	v_add_f32_e32 v13, 1.0, v13
	v_rcp_f32_e32 v10, v10
	v_rcp_f32_e32 v11, v11
	v_rcp_f32_e32 v12, v12
	v_rcp_f32_e32 v13, v13
	s_waitcnt vmcnt(1)
	v_cvt_f32_f16_e32 v20, v14
	v_fma_f32 v10, v10, -2.0, 1.0
	v_fma_f32 v11, v11, -2.0, 1.0
	v_cvt_f32_f16_sdwa v14, v14 dst_sel:DWORD dst_unused:UNUSED_PAD src0_sel:WORD_1
	v_fma_f32 v12, v12, -2.0, 1.0
	v_fma_f32 v13, v13, -2.0, 1.0
	v_cvt_pk_f16_f32 v10, v10, v11
	v_cvt_pk_f16_f32 v11, v12, v13
	v_add_u32_e32 v13, s1, v212
	v_exp_f32_e32 v12, v20
	ds_write_b64 v13, v[10:11]
	v_cvt_f32_f16_e32 v11, v15
	v_cvt_f32_f16_sdwa v13, v15 dst_sel:DWORD dst_unused:UNUSED_PAD src0_sel:WORD_1
	v_add_f32_e32 v10, 1.0, v12
	v_exp_f32_e32 v12, v14
	v_exp_f32_e32 v14, v11
	v_exp_f32_e32 v13, v13
	v_rcp_f32_e32 v10, v10
	v_add_f32_e32 v11, 1.0, v12
	v_add_f32_e32 v12, 1.0, v14
	v_add_f32_e32 v13, 1.0, v13
	v_rcp_f32_e32 v11, v11
	v_rcp_f32_e32 v12, v12
	v_rcp_f32_e32 v13, v13
	v_cvt_f32_f16_e32 v14, v16
	v_fma_f32 v10, v10, -2.0, 1.0
	v_fma_f32 v11, v11, -2.0, 1.0
	v_add_co_u32_e32 v150, vcc, s2, v18
	v_fma_f32 v12, v12, -2.0, 1.0
	v_fma_f32 v13, v13, -2.0, 1.0
	v_cvt_pk_f16_f32 v10, v10, v11
	v_cvt_pk_f16_f32 v11, v12, v13
	v_exp_f32_e32 v12, v14
	v_cvt_f32_f16_sdwa v14, v16 dst_sel:DWORD dst_unused:UNUSED_PAD src0_sel:WORD_1
	v_add_u32_e32 v13, s1, v210
	ds_write_b64 v13, v[10:11]
	v_add_f32_e32 v10, 1.0, v12
	v_cvt_f32_f16_e32 v11, v17
	v_exp_f32_e32 v12, v14
	v_cvt_f32_f16_sdwa v13, v17 dst_sel:DWORD dst_unused:UNUSED_PAD src0_sel:WORD_1
	v_rcp_f32_e32 v10, v10
	v_exp_f32_e32 v14, v11
	v_add_f32_e32 v11, 1.0, v12
	v_exp_f32_e32 v12, v13
	v_rcp_f32_e32 v11, v11
	v_add_f32_e32 v13, 1.0, v14
	v_bitop3_b32 v1, v33, v32, 10 bitop3:0x36
	v_add_f32_e32 v12, 1.0, v12
	v_rcp_f32_e32 v146, v13
	v_rcp_f32_e32 v147, v12
	v_fma_f32 v148, v10, -2.0, 1.0
	v_fma_f32 v149, v11, -2.0, 1.0
	global_load_dwordx4 v[10:13], v[22:23], off
	global_load_dwordx4 v[14:17], v[22:23], off offset:1024
	v_addc_co_u32_e32 v151, vcc, 0, v19, vcc
	global_load_dwordx4 v[18:21], v[22:23], off offset:2048
	s_nop 0
	global_load_dwordx4 v[22:25], v[22:23], off offset:3072
	s_nop 0
	global_load_dwordx4 v[26:29], v[34:35], off offset:1024
	global_load_dwordx4 v[30:33], v[34:35], off offset:2048
	s_nop 0
	global_load_dwordx4 v[34:37], v[34:35], off offset:3072
	s_nop 0
	global_load_dwordx4 v[38:41], v[46:47], off offset:1024
	global_load_dwordx4 v[42:45], v[46:47], off offset:2048
	s_nop 0
	global_load_dwordx4 v[46:49], v[46:47], off offset:3072
	s_nop 0
	global_load_dwordx4 v[50:53], v[66:67], off offset:-4096
	global_load_dwordx4 v[54:57], v[66:67], off
	global_load_dwordx4 v[58:61], v[66:67], off offset:1024
	global_load_dwordx4 v[62:65], v[66:67], off offset:2048
	s_nop 0
	global_load_dwordx4 v[66:69], v[66:67], off offset:3072
	s_nop 0
	global_load_dwordx4 v[70:73], v[86:87], off offset:-4096
	global_load_dwordx4 v[74:77], v[86:87], off
	global_load_dwordx4 v[78:81], v[86:87], off offset:1024
	global_load_dwordx4 v[82:85], v[86:87], off offset:2048
	s_nop 0
	global_load_dwordx4 v[86:89], v[86:87], off offset:3072
	s_nop 0
	global_load_dwordx4 v[90:93], v[106:107], off offset:-4096
	global_load_dwordx4 v[94:97], v[106:107], off
	global_load_dwordx4 v[98:101], v[106:107], off offset:1024
	global_load_dwordx4 v[102:105], v[106:107], off offset:2048
	s_nop 0
	global_load_dwordx4 v[106:109], v[106:107], off offset:3072
	s_nop 0
	global_load_dwordx4 v[110:113], v[110:111], off offset:-4096
	s_nop 0
	global_load_dwordx4 v[114:117], v[122:123], off offset:1024
	global_load_dwordx4 v[118:121], v[122:123], off offset:2048
	s_nop 0
	global_load_dwordx4 v[122:125], v[122:123], off offset:3072
	s_nop 0
	global_load_dwordx4 v[126:129], v[134:135], off offset:1024
	global_load_dwordx4 v[130:133], v[134:135], off offset:2048
	s_nop 0
	global_load_dwordx4 v[134:137], v[134:135], off offset:3072
	s_nop 0
	global_load_dwordx4 v[178:181], v[150:151], off
	global_load_dwordx4 v[174:177], v[150:151], off offset:64
	global_load_dwordx4 v[170:173], v[150:151], off offset:128
	global_load_dwordx4 v[202:205], v[150:151], off offset:192
	s_waitcnt vmcnt(36)
	v_cvt_f32_f16_e32 v155, v138
	v_cvt_f32_f16_sdwa v138, v138 dst_sel:DWORD dst_unused:UNUSED_PAD src0_sel:WORD_1
	v_fma_f32 v146, v146, -2.0, 1.0
	v_fma_f32 v147, v147, -2.0, 1.0
	v_cvt_pk_f16_f32 v148, v148, v149
	v_exp_f32_e32 v150, v155
	v_cvt_pk_f16_f32 v149, v146, v147
	v_cvt_f32_f16_e32 v147, v139
	v_cvt_f32_f16_sdwa v139, v139 dst_sel:DWORD dst_unused:UNUSED_PAD src0_sel:WORD_1
	v_add_f32_e32 v146, 1.0, v150
	v_exp_f32_e32 v150, v138
	v_rcp_f32_e32 v138, v146
	v_exp_f32_e32 v146, v147
	v_lshl_add_u32 v1, v1, 4, v152
	v_add_f32_e32 v147, 1.0, v150
	v_exp_f32_e32 v150, v139
	v_rcp_f32_e32 v139, v147
	v_add_f32_e32 v146, 1.0, v146
	v_rcp_f32_e32 v146, v146
	v_add_f32_e32 v147, 1.0, v150
	v_rcp_f32_e32 v147, v147
	v_fma_f32 v138, v138, -2.0, 1.0
	v_fma_f32 v139, v139, -2.0, 1.0
	v_add_u32_e32 v151, s1, v1
	v_cvt_pk_f16_f32 v138, v138, v139
	v_fma_f32 v146, v146, -2.0, 1.0
	v_fma_f32 v147, v147, -2.0, 1.0
	ds_write_b64 v151, v[148:149]
	v_cvt_pk_f16_f32 v139, v146, v147
	v_cvt_f32_f16_e32 v146, v140
	v_cvt_f32_f16_sdwa v140, v140 dst_sel:DWORD dst_unused:UNUSED_PAD src0_sel:WORD_1
	v_cvt_f32_f16_e32 v147, v141
	v_cvt_f32_f16_sdwa v141, v141 dst_sel:DWORD dst_unused:UNUSED_PAD src0_sel:WORD_1
	v_exp_f32_e32 v146, v146
	v_exp_f32_e32 v148, v140
	v_lshl_add_u32 v216, v153, 4, v152
	v_lshl_add_u32 v214, v154, 4, v152
	v_add_f32_e32 v140, 1.0, v146
	v_exp_f32_e32 v146, v147
	v_add_f32_e32 v147, 1.0, v148
	v_exp_f32_e32 v148, v141
	v_rcp_f32_e32 v141, v147
	v_add_f32_e32 v146, 1.0, v146
	v_rcp_f32_e32 v140, v140
	v_add_f32_e32 v147, 1.0, v148
	v_rcp_f32_e32 v146, v146
	v_rcp_f32_e32 v147, v147
	v_add_u32_e32 v148, s1, v216
	ds_write_b64 v148, v[138:139]
	v_fma_f32 v138, v140, -2.0, 1.0
	v_fma_f32 v139, v141, -2.0, 1.0
	v_fma_f32 v140, v146, -2.0, 1.0
	v_fma_f32 v141, v147, -2.0, 1.0
	v_cvt_pk_f16_f32 v138, v138, v139
	v_cvt_pk_f16_f32 v139, v140, v141
	v_add_u32_e32 v140, s1, v214
	s_lshl_b32 s2, s12, 7
	s_add_i32 s1, 0, 0x20000
	s_add_u32 s0, s4, s0
	ds_write_b64 v140, v[138:139]
	v_add_u32_e32 v219, s1, v143
	v_bitop3_b32 v138, v218, v0, 15 bitop3:0x78
	s_addc_u32 s1, s5, 0
	v_lshlrev_b32_e32 v220, 4, v138
	v_lshl_add_u64 v[138:139], s[0:1], 0, v[144:145]
	s_mov_b64 s[0:1], 0x800080
	s_waitcnt lgkmcnt(0)
	s_barrier
	v_lshl_add_u64 v[208:209], v[138:139], 0, s[0:1]
	s_waitcnt vmcnt(0)
	v_mov_b32_e32 v232, v170
	v_mov_b32_e32 v233, v171
	v_mov_b32_e32 v234, v172
	v_mov_b32_e32 v235, v173
	v_mov_b32_e32 v236, v202
	v_mov_b32_e32 v237, v203
	v_mov_b32_e32 v238, v204
	v_mov_b32_e32 v239, v205
	v_cvt_f32_f16_e32 v198, v178
	v_cvt_f32_f16_sdwa v199, v178 dst_sel:DWORD dst_unused:UNUSED_PAD src0_sel:WORD_1
	v_cvt_f32_f16_e32 v200, v179
	v_cvt_f32_f16_sdwa v201, v179 dst_sel:DWORD dst_unused:UNUSED_PAD src0_sel:WORD_1
	v_cvt_f32_f16_e32 v194, v180
	v_cvt_f32_f16_sdwa v195, v180 dst_sel:DWORD dst_unused:UNUSED_PAD src0_sel:WORD_1
	v_cvt_f32_f16_e32 v196, v181
	v_cvt_f32_f16_sdwa v197, v181 dst_sel:DWORD dst_unused:UNUSED_PAD src0_sel:WORD_1
	v_cvt_f32_f16_e32 v190, v174
	v_cvt_f32_f16_sdwa v191, v174 dst_sel:DWORD dst_unused:UNUSED_PAD src0_sel:WORD_1
	v_cvt_f32_f16_e32 v192, v175
	v_cvt_f32_f16_sdwa v193, v175 dst_sel:DWORD dst_unused:UNUSED_PAD src0_sel:WORD_1
	v_cvt_f32_f16_e32 v186, v176
	v_cvt_f32_f16_sdwa v187, v176 dst_sel:DWORD dst_unused:UNUSED_PAD src0_sel:WORD_1
	v_cvt_f32_f16_e32 v188, v177
	v_cvt_f32_f16_sdwa v189, v177 dst_sel:DWORD dst_unused:UNUSED_PAD src0_sel:WORD_1
	s_mov_b64 s[0:1], 0x400000
	v_xor_b32_e32 v221, 64, v220
	v_xor_b32_e32 v222, 0x80, v220
	v_xor_b32_e32 v223, 0xc0, v220
	ds_read_b128 v[154:157], v213 offset:0
	ds_read_b128 v[158:161], v213 offset:1024
	ds_read_b128 v[162:165], v213 offset:2048
	ds_read_b128 v[166:169], v213 offset:3072
	s_waitcnt lgkmcnt(0)

_Z12final_kernelPKfS0_S0_Pf:
	s_load_dwordx4 s[4:7], s[0:1], 0x0
	v_and_b32_e32 v22, 63, v0
	v_lshrrev_b32_e32 v0, 6, v0
	v_lshl_or_b32 v0, s2, 2, v0
	v_ashrrev_i32_e32 v1, 31, v0
	v_lshlrev_b64 v[2:3], 11, v[0:1]
	s_waitcnt lgkmcnt(0)
	v_lshl_add_u64 v[2:3], s[4:5], 0, v[2:3]
	v_lshlrev_b32_e32 v18, 5, v22
	v_mov_b32_e32 v19, 0
	v_lshl_add_u64 v[20:21], v[2:3], 0, v[18:19]
	global_load_dwordx4 v[2:5], v[20:21], off
	global_load_dwordx4 v[6:9], v18, s[6:7]
	global_load_dwordx4 v[10:13], v18, s[6:7] offset:16
	global_load_dwordx4 v[14:17], v[20:21], off offset:16
	v_mbcnt_lo_u32_b32 v18, -1, 0
	v_mbcnt_hi_u32_b32 v18, -1, v18
	v_and_b32_e32 v19, 64, v18
	v_xor_b32_e32 v20, 32, v18
	v_add_u32_e32 v19, 64, v19
	v_cmp_lt_i32_e32 vcc, v20, v19
	s_waitcnt vmcnt(2)
	v_mul_f32_e32 v3, v3, v7
	v_fmac_f32_e32 v3, v2, v6
	v_fmac_f32_e32 v3, v4, v8
	v_fmac_f32_e32 v3, v5, v9
	s_waitcnt vmcnt(0)
	v_fmac_f32_e32 v3, v14, v10
	v_fmac_f32_e32 v3, v15, v11
	v_cndmask_b32_e32 v20, v18, v20, vcc
	v_fmac_f32_e32 v3, v16, v12
	v_lshlrev_b32_e32 v20, 2, v20
	v_fmac_f32_e32 v3, v17, v13
	ds_bpermute_b32 v2, v20, v3
	v_xor_b32_e32 v4, 16, v18
	v_cmp_lt_i32_e32 vcc, v4, v19
	s_waitcnt lgkmcnt(0)
	v_add_f32_e32 v2, v3, v2
	v_cndmask_b32_e32 v4, v18, v4, vcc
	v_lshlrev_b32_e32 v4, 2, v4
	ds_bpermute_b32 v3, v4, v2
	v_xor_b32_e32 v4, 8, v18
	v_cmp_lt_i32_e32 vcc, v4, v19
	s_waitcnt lgkmcnt(0)
	v_add_f32_e32 v2, v2, v3
	v_cndmask_b32_e32 v4, v18, v4, vcc
	v_lshlrev_b32_e32 v4, 2, v4
	ds_bpermute_b32 v3, v4, v2
	v_xor_b32_e32 v4, 4, v18
	v_cmp_lt_i32_e32 vcc, v4, v19
	s_waitcnt lgkmcnt(0)
	v_add_f32_e32 v2, v2, v3
	v_cndmask_b32_e32 v4, v18, v4, vcc
	v_lshlrev_b32_e32 v4, 2, v4
	ds_bpermute_b32 v3, v4, v2
	v_xor_b32_e32 v4, 2, v18
	v_cmp_lt_i32_e32 vcc, v4, v19
	s_waitcnt lgkmcnt(0)
	v_add_f32_e32 v2, v2, v3
	v_cndmask_b32_e32 v4, v18, v4, vcc
	v_lshlrev_b32_e32 v4, 2, v4
	ds_bpermute_b32 v3, v4, v2
	v_xor_b32_e32 v4, 1, v18
	v_cmp_lt_i32_e32 vcc, v4, v19
	s_waitcnt lgkmcnt(0)
	v_add_f32_e32 v2, v2, v3
	v_cndmask_b32_e32 v4, v18, v4, vcc
	v_lshlrev_b32_e32 v3, 2, v4
	ds_bpermute_b32 v3, v3, v2
	v_cmp_eq_u32_e32 vcc, 0, v22
	s_and_saveexec_b64 s[2:3], vcc
	s_cbranch_execz .LBB6_2
	s_load_dwordx4 s[0:3], s[0:1], 0x10
	s_waitcnt lgkmcnt(0)
	v_add_f32_e32 v2, v2, v3
	s_mov_b32 s4, 0xb2a5705f
	s_mov_b32 s5, 0x42ce8ed0
	v_mov_b32_e32 v17, 0x7f800000
	s_load_dword s0, s[0:1], 0x0
	s_mov_b32 s1, 0xbfb8aa3b
	v_lshl_add_u64 v[0:1], v[0:1], 2, s[2:3]
	s_waitcnt lgkmcnt(0)
	v_add_f32_e32 v2, s0, v2
	v_mul_f32_e64 v3, |v2|, s1
	v_fma_f32 v4, |v2|, s1, -v3
	v_rndne_f32_e32 v5, v3
	v_fma_f32 v4, |v2|, s4, v4
	v_sub_f32_e32 v3, v3, v5
	v_add_f32_e32 v3, v3, v4
	v_cvt_i32_f32_e32 v5, v5
	v_exp_f32_e32 v3, v3
	s_mov_b32 s0, 0xc2b17218
	v_cmp_ngt_f32_e64 vcc, |v2|, s5
	v_max_f32_e32 v16, 0, v2
	v_ldexp_f32 v3, v3, v5
	v_cndmask_b32_e32 v3, 0, v3, vcc
	v_cmp_nlt_f32_e64 vcc, |v2|, s0
	s_mov_b32 s0, 0x3f2aaaab
	s_mov_b32 s1, 0x7f800000
	v_cndmask_b32_e32 v18, v17, v3, vcc
	v_add_f32_e32 v4, 1.0, v18
	v_add_f32_e32 v2, -1.0, v4
	v_sub_f32_e32 v3, v2, v4
	v_add_f32_e32 v3, 1.0, v3
	v_sub_f32_e32 v2, v18, v2
	v_add_f32_e32 v5, v2, v3
	v_frexp_mant_f32_e32 v6, v4
	v_cvt_f64_f32_e32 v[2:3], v4
	v_frexp_exp_i32_f64_e32 v2, v[2:3]
	v_cmp_gt_f32_e32 vcc, s0, v6
	s_mov_b32 s0, 0x3f317218
	s_nop 0
	v_subbrev_co_u32_e32 v10, vcc, 0, v2, vcc
	v_sub_u32_e32 v2, 0, v10
	v_ldexp_f32 v3, v4, v2
	v_add_f32_e32 v4, -1.0, v3
	v_add_f32_e32 v6, 1.0, v3
	v_ldexp_f32 v2, v5, v2
	v_add_f32_e32 v5, 1.0, v4
	v_add_f32_e32 v7, -1.0, v6
	v_sub_f32_e32 v5, v3, v5
	v_sub_f32_e32 v3, v3, v7
	v_add_f32_e32 v5, v2, v5
	v_add_f32_e32 v2, v2, v3
	v_add_f32_e32 v11, v6, v2
	v_rcp_f32_e32 v13, v11
	v_sub_f32_e32 v3, v6, v11
	v_add_f32_e32 v12, v2, v3
	v_add_f32_e32 v3, v4, v5
	v_mul_f32_e32 v15, v3, v13
	v_sub_f32_e32 v2, v4, v3
	v_mul_f32_e32 v4, v11, v15
	v_fma_f32 v6, v15, v11, -v4
	v_fmac_f32_e32 v6, v15, v12
	v_add_f32_e32 v14, v5, v2
	v_add_f32_e32 v2, v4, v6
	v_sub_f32_e32 v5, v3, v2
	v_pk_add_f32 v[8:9], v[2:3], v[4:5] neg_lo:[0,1] neg_hi:[0,1]
	v_mov_b32_e32 v7, v2
	v_pk_add_f32 v[2:3], v[8:9], v[6:7] neg_lo:[0,1] neg_hi:[0,1]
	v_cmp_neq_f32_e32 vcc, s1, v18
	v_add_f32_e32 v3, v14, v3
	v_add_f32_e32 v2, v2, v3
	v_add_f32_e32 v3, v5, v2
	v_mul_f32_e32 v14, v13, v3
	v_mul_f32_e32 v4, v11, v14
	v_fma_f32 v6, v14, v11, -v4
	v_fmac_f32_e32 v6, v14, v12
	v_sub_f32_e32 v5, v5, v3
	v_add_f32_e32 v11, v2, v5
	v_add_f32_e32 v2, v4, v6
	v_sub_f32_e32 v5, v3, v2
	v_pk_add_f32 v[8:9], v[2:3], v[4:5] neg_lo:[0,1] neg_hi:[0,1]
	v_mov_b32_e32 v7, v2
	v_pk_add_f32 v[2:3], v[8:9], v[6:7] neg_lo:[0,1] neg_hi:[0,1]
	v_cvt_f32_i32_e32 v4, v10
	v_add_f32_e32 v3, v11, v3
	v_add_f32_e32 v2, v2, v3
	v_add_f32_e32 v2, v5, v2
	v_add_f32_e32 v5, v15, v14
	v_sub_f32_e32 v3, v5, v15
	v_mul_f32_e32 v2, v13, v2
	v_sub_f32_e32 v3, v14, v3
	v_add_f32_e32 v2, v3, v2
	v_add_f32_e32 v6, v5, v2
	v_mul_f32_e32 v8, v6, v6
	v_mov_b32_e32 v3, 0x3ecc95a3
	v_sub_f32_e32 v5, v6, v5
	v_fmac_f32_e32 v3, 0x3e9b6dac, v8
	v_sub_f32_e32 v2, v2, v5
	v_fmaak_f32 v3, v8, v3, 0x3f2aaada
	v_ldexp_f32 v9, v2, 1
	v_mul_f32_e32 v5, v6, v8
	v_mov_b32_e32 v2, 0x3f317218
	v_pk_mul_f32 v[2:3], v[4:5], v[2:3]
	v_ldexp_f32 v7, v6, 1
	v_fma_f32 v5, v4, s0, -v2
	v_fmamk_f32 v6, v4, 0xb102e308, v5
	v_add_f32_e32 v4, v2, v6
	v_add_f32_e32 v5, v3, v7
	v_mov_b32_e32 v8, v2
	v_sub_f32_e32 v7, v5, v7
	v_sub_f32_e32 v7, v3, v7
	v_add_f32_e32 v9, v9, v7
	v_pk_add_f32 v[2:3], v[4:5], v[2:3] neg_lo:[0,1] neg_hi:[0,1]
	v_add_f32_e32 v10, v4, v8
	v_add_f32_e32 v11, v5, v9
	v_mov_b32_e32 v7, v4
	v_mov_b32_e32 v3, v11
	v_pk_add_f32 v[12:13], v[6:7], v[2:3] neg_lo:[0,1] neg_hi:[0,1]
	v_add_f32_e32 v2, v6, v2
	v_add_f32_e32 v3, v7, v3
	v_mov_b32_e32 v8, v9
	v_pk_add_f32 v[6:7], v[2:3], v[4:5] op_sel:[1,0] op_sel_hi:[0,1] neg_lo:[0,1] neg_hi:[0,1]
	v_pk_add_f32 v[14:15], v[10:11], v[6:7] op_sel_hi:[1,0] neg_lo:[0,1] neg_hi:[0,1]
	v_mov_b32_e32 v10, v11
	v_mov_b32_e32 v11, v3
	v_pk_mov_b32 v[6:7], v[4:5], v[6:7] op_sel:[1,0]
	v_mov_b32_e32 v9, v4
	v_pk_add_f32 v[6:7], v[10:11], v[6:7] neg_lo:[0,1] neg_hi:[0,1]
	v_mov_b32_e32 v14, v12
	v_pk_add_f32 v[4:5], v[8:9], v[6:7] neg_lo:[0,1] neg_hi:[0,1]
	v_mov_b32_e32 v13, v3
	v_add_f32_e32 v6, v14, v4
	v_add_f32_e32 v7, v15, v5
	s_mov_b32 s0, 0x33800000
	v_pk_add_f32 v[8:9], v[6:7], v[6:7] op_sel:[0,1] op_sel_hi:[1,0]
	s_nop 0
	v_pk_add_f32 v[2:3], v[2:3], v[8:9] op_sel:[1,0] op_sel_hi:[0,1]
	v_mov_b32_e32 v7, v2
	v_pk_add_f32 v[10:11], v[6:7], v[12:13] neg_lo:[0,1] neg_hi:[0,1]
	v_mov_b32_e32 v5, v8
	v_sub_f32_e32 v3, v6, v10
	v_pk_add_f32 v[4:5], v[4:5], v[10:11] neg_lo:[0,1] neg_hi:[0,1]
	v_sub_f32_e32 v3, v12, v3
	v_add_f32_e32 v3, v4, v3
	v_add_f32_e32 v3, v3, v5
	v_add_f32_e32 v2, v2, v3
	v_cndmask_b32_e32 v2, v17, v2, vcc
	v_cmp_lt_f32_e64 vcc, |v18|, s0
	s_nop 1
	v_cndmask_b32_e32 v2, v2, v18, vcc
	v_add_f32_e32 v2, v16, v2
	global_store_dword v[0:1], v2, off

.LBB7_11:
	v_lshlrev_b32_e32 v0, 2, v56
	v_lshl_or_b32 v0, s13, 5, v0
	v_or_b32_e32 v26, s11, v0
	v_ashrrev_i32_e32 v27, 31, v26
	s_waitcnt lgkmcnt(0)
	v_lshl_add_u64 v[28:29], v[26:27], 2, s[4:5]
	global_load_dwordx4 v[18:21], v[28:29], off
	global_load_dwordx4 v[22:25], v[28:29], off offset:64
	s_load_dword s4, s[0:1], 0x28
	s_lshl_b32 s0, s12, 5
	s_add_i32 s0, s0, s10
	v_or_b32_e32 v28, s0, v1
	v_or_b32_e32 v29, 16, v28
	v_lshl_add_u64 v[0:1], v[26:27], 1, s[2:3]
	s_waitcnt lgkmcnt(0)
	v_mad_i64_i32 v[26:27], s[0:1], v28, s4, 0
	v_mad_i64_i32 v[28:29], s[0:1], v29, s4, 0
	v_lshl_add_u64 v[26:27], v[26:27], 1, v[0:1]
	v_lshl_add_u64 v[0:1], v[28:29], 1, v[0:1]
	s_waitcnt vmcnt(0)
	v_add_f32_e32 v12, v20, v12
	v_add_f32_e32 v13, v21, v13
	v_add_f32_e32 v10, v18, v10
	v_add_f32_e32 v11, v19, v11
	v_add_f32_e32 v16, v20, v16
	v_add_f32_e32 v17, v21, v17
	v_add_f32_e32 v14, v18, v14
	v_add_f32_e32 v15, v19, v15
	v_add_f32_e32 v8, v24, v8
	v_add_f32_e32 v9, v25, v9
	v_add_f32_e32 v6, v22, v6
	v_add_f32_e32 v7, v23, v7
	v_add_f32_e32 v4, v24, v4
	v_add_f32_e32 v5, v25, v5
	v_add_f32_e32 v2, v22, v2
	v_add_f32_e32 v3, v23, v3
	v_cvt_pk_f16_f32 v13, v12, v13
	v_cvt_pk_f16_f32 v12, v10, v11
	v_cvt_pk_f16_f32 v11, v16, v17
	v_cvt_pk_f16_f32 v10, v14, v15
	v_cvt_pk_f16_f32 v9, v8, v9
	v_cvt_pk_f16_f32 v8, v6, v7
	v_cvt_pk_f16_f32 v5, v4, v5
	v_cvt_pk_f16_f32 v4, v2, v3
	global_store_dwordx2 v[26:27], v[12:13], off
	global_store_dwordx2 v[0:1], v[10:11], off
	global_store_dwordx2 v[26:27], v[8:9], off offset:32
	global_store_dwordx2 v[0:1], v[4:5], off offset:32
	s_endpgm
	.p2align	8

.LBB8_20:
	v_lshl_or_b32 v170, s58, 8, v187
	v_ashrrev_i32_e32 v171, 31, v170
	v_lshl_add_u64 v[146:147], v[170:171], 2, s[14:15]
	global_load_dwordx4 v[158:161], v[146:147], off
	global_load_dwordx4 v[154:157], v[146:147], off offset:16
	global_load_dwordx4 v[150:153], v[146:147], off offset:512
	s_nop 0
	global_load_dwordx4 v[146:149], v[146:147], off offset:528
	s_lshl_b32 s34, s57, 8
	s_add_i32 s34, s34, s50
	s_ashr_i32 s35, s34, 4
	v_add_u32_e32 v193, s35, v166
	s_waitcnt lgkmcnt(0)
	v_mad_i64_i32 v[194:195], s[58:59], v193, s29, 0
	v_add_u32_e32 v196, 1, v193
	v_lshlrev_b64 v[170:171], 1, v[170:171]
	v_add_u32_e32 v198, 2, v193
	v_lshl_add_u64 v[194:195], v[194:195], 1, s[12:13]
	v_mad_i64_i32 v[196:197], s[58:59], v196, s29, 0
	v_mad_i64_i32 v[198:199], s[58:59], v198, s29, 0
	v_lshl_add_u64 v[194:195], v[194:195], 0, v[170:171]
	v_lshl_add_u64 v[196:197], v[196:197], 1, s[12:13]
	v_lshl_add_u64 v[198:199], v[198:199], 1, s[12:13]
	v_lshl_add_u64 v[196:197], v[196:197], 0, v[170:171]
	v_lshl_add_u64 v[198:199], v[198:199], 0, v[170:171]
	s_add_i32 s35, s34, 0x80
	s_ashr_i32 s35, s35, 4
	s_mov_b64 vcc, s[4:5]
	s_waitcnt vmcnt(0)
	v_add_f32_e32 v140, v140, v160
	v_add_f32_e32 v141, v141, v161
	v_add_f32_e32 v138, v138, v158
	v_add_f32_e32 v139, v139, v159
	v_add_f32_e32 v144, v144, v156
	v_add_f32_e32 v145, v145, v157
	v_add_f32_e32 v142, v142, v154
	v_add_f32_e32 v143, v143, v155
	v_add_f32_e32 v136, v136, v152
	v_add_f32_e32 v137, v137, v153
	v_add_f32_e32 v134, v134, v150
	v_add_f32_e32 v135, v135, v151
	v_add_f32_e32 v132, v132, v148
	v_add_f32_e32 v133, v133, v149
	v_add_f32_e32 v130, v130, v146
	v_add_f32_e32 v131, v131, v147
	v_add_f32_e32 v128, v128, v160
	v_add_f32_e32 v129, v129, v161
	v_add_f32_e32 v126, v126, v158
	v_add_f32_e32 v127, v127, v159
	v_add_f32_e32 v124, v124, v156
	v_add_f32_e32 v125, v125, v157
	v_add_f32_e32 v122, v122, v154
	v_add_f32_e32 v123, v123, v155
	v_add_f32_e32 v120, v120, v152
	v_add_f32_e32 v121, v121, v153
	v_add_f32_e32 v118, v118, v150
	v_add_f32_e32 v119, v119, v151
	v_add_f32_e32 v116, v116, v148
	v_add_f32_e32 v117, v117, v149
	v_add_f32_e32 v114, v114, v146
	v_add_f32_e32 v115, v115, v147
	v_add_f32_e32 v108, v108, v156
	v_add_f32_e32 v109, v109, v157
	v_add_f32_e32 v106, v106, v154
	v_add_f32_e32 v107, v107, v155
	v_mul_f32_e32 v140, s28, v140
	v_mul_f32_e32 v141, s28, v141
	v_mul_f32_e32 v138, s28, v138
	v_mul_f32_e32 v139, s28, v139
	v_mul_f32_e32 v144, s28, v144
	v_mul_f32_e32 v145, s28, v145
	v_mul_f32_e32 v142, s28, v142
	v_mul_f32_e32 v143, s28, v143
	v_add_f32_e32 v112, v112, v160
	v_add_f32_e32 v113, v113, v161
	v_add_f32_e32 v110, v110, v158
	v_add_f32_e32 v111, v111, v159
	v_mul_f32_e32 v136, s28, v136
	v_mul_f32_e32 v137, s28, v137
	v_mul_f32_e32 v134, s28, v134
	v_mul_f32_e32 v135, s28, v135
	v_mul_f32_e32 v132, s28, v132
	v_mul_f32_e32 v133, s28, v133
	v_mul_f32_e32 v130, s28, v130
	v_mul_f32_e32 v131, s28, v131
	v_mul_f32_e32 v128, s28, v128
	v_mul_f32_e32 v129, s28, v129
	v_mul_f32_e32 v126, s28, v126
	v_mul_f32_e32 v127, s28, v127
	v_mul_f32_e32 v124, s28, v124
	v_mul_f32_e32 v125, s28, v125
	v_mul_f32_e32 v122, s28, v122
	v_mul_f32_e32 v123, s28, v123
	v_mul_f32_e32 v200, s28, v120
	v_mul_f32_e32 v201, s28, v121
	v_mul_f32_e32 v202, s28, v118
	v_mul_f32_e32 v203, s28, v119
	v_mul_f32_e32 v118, s28, v116
	v_mul_f32_e32 v119, s28, v117
	v_mul_f32_e32 v204, s28, v114
	v_mul_f32_e32 v205, s28, v115
	v_mul_f32_e32 v210, s28, v108
	v_mul_f32_e32 v211, s28, v109
	v_mul_f32_e32 v212, s28, v106
	v_mul_f32_e32 v213, s28, v107
	v_cvt_pk_f16_f32 v109, v144, v145
	v_cvt_pk_f16_f32 v107, v140, v141
	v_cvt_pk_f16_f32 v108, v142, v143
	v_cvt_pk_f16_f32 v106, v138, v139
	v_add_f32_e32 v104, v104, v152
	v_add_f32_e32 v105, v105, v153
	v_add_f32_e32 v102, v102, v150
	v_add_f32_e32 v103, v103, v151
	v_add_f32_e32 v100, v100, v148
	v_add_f32_e32 v101, v101, v149
	v_add_f32_e32 v98, v98, v146
	v_add_f32_e32 v99, v99, v147
	v_mul_f32_e32 v206, s28, v112
	v_mul_f32_e32 v207, s28, v113
	v_mul_f32_e32 v208, s28, v110
	v_mul_f32_e32 v209, s28, v111
	v_cvt_pk_f16_f32 v113, v132, v133
	v_cvt_pk_f16_f32 v111, v136, v137
	v_cvt_pk_f16_f32 v112, v130, v131
	v_cvt_pk_f16_f32 v110, v134, v135
	v_cvt_pk_f16_f32 v117, v124, v125
	v_cvt_pk_f16_f32 v115, v128, v129
	v_cvt_pk_f16_f32 v116, v122, v123
	v_cvt_pk_f16_f32 v114, v126, v127
	v_cvt_pk_f16_f32 v121, v118, v119
	v_cvt_pk_f16_f32 v119, v200, v201
	v_cvt_pk_f16_f32 v120, v204, v205
	v_cvt_pk_f16_f32 v118, v202, v203
	global_store_dwordx4 v[194:195], v[106:109], off
	global_store_dwordx4 v[194:195], v[110:113], off offset:256
	global_store_dwordx4 v[196:197], v[114:117], off
	global_store_dwordx4 v[196:197], v[118:121], off offset:256
	v_mul_f32_e32 v104, s28, v104
	v_mul_f32_e32 v105, s28, v105
	v_mul_f32_e32 v102, s28, v102
	v_mul_f32_e32 v103, s28, v103
	v_mul_f32_e32 v100, s28, v100
	v_mul_f32_e32 v101, s28, v101
	v_mul_f32_e32 v106, s28, v98
	v_mul_f32_e32 v107, s28, v99
	v_cvt_pk_f16_f32 v101, v100, v101
	v_cvt_pk_f16_f32 v99, v104, v105
	v_cvt_pk_f16_f32 v100, v106, v107
	v_cvt_pk_f16_f32 v98, v102, v103
	global_store_dwordx4 v[198:199], v[98:101], off offset:256
	v_add_f32_e32 v96, v96, v160
	v_add_f32_e32 v97, v97, v161
	v_add_f32_e32 v94, v94, v158
	v_add_f32_e32 v95, v95, v159
	v_add_u32_e32 v98, 3, v193
	v_mad_i64_i32 v[98:99], s[58:59], v98, s29, 0
	v_add_f32_e32 v92, v92, v156
	v_add_f32_e32 v93, v93, v157
	v_add_f32_e32 v90, v90, v154
	v_add_f32_e32 v91, v91, v155
	v_lshl_add_u64 v[98:99], v[98:99], 1, s[12:13]
	v_mul_f32_e32 v96, s28, v96
	v_mul_f32_e32 v97, s28, v97
	v_mul_f32_e32 v94, s28, v94
	v_mul_f32_e32 v95, s28, v95
	v_mul_f32_e32 v92, s28, v92
	v_mul_f32_e32 v93, s28, v93
	v_mul_f32_e32 v100, s28, v90
	v_mul_f32_e32 v101, s28, v91
	v_cvt_pk_f16_f32 v123, v210, v211
	v_cvt_pk_f16_f32 v121, v206, v207
	v_cvt_pk_f16_f32 v122, v212, v213
	v_cvt_pk_f16_f32 v120, v208, v209
	v_lshl_add_u64 v[98:99], v[98:99], 0, v[170:171]
	v_cvt_pk_f16_f32 v93, v92, v93
	v_cvt_pk_f16_f32 v91, v96, v97
	v_cvt_pk_f16_f32 v92, v100, v101
	v_cvt_pk_f16_f32 v90, v94, v95
	v_add_f32_e32 v88, v88, v152
	v_add_f32_e32 v89, v89, v153
	v_add_f32_e32 v86, v86, v150
	v_add_f32_e32 v87, v87, v151
	v_add_f32_e32 v84, v84, v148
	v_add_f32_e32 v85, v85, v149
	v_add_f32_e32 v82, v82, v146
	v_add_f32_e32 v83, v83, v147
	global_store_dwordx4 v[198:199], v[120:123], off
	global_store_dwordx4 v[98:99], v[90:93], off
	v_mul_f32_e32 v88, s28, v88
	v_mul_f32_e32 v89, s28, v89
	v_mul_f32_e32 v86, s28, v86
	v_mul_f32_e32 v87, s28, v87
	v_mul_f32_e32 v84, s28, v84
	v_mul_f32_e32 v85, s28, v85
	v_mul_f32_e32 v90, s28, v82
	v_mul_f32_e32 v91, s28, v83
	v_cvt_pk_f16_f32 v85, v84, v85
	v_cvt_pk_f16_f32 v83, v88, v89
	v_cvt_pk_f16_f32 v84, v90, v91
	v_cvt_pk_f16_f32 v82, v86, v87
	global_store_dwordx4 v[98:99], v[82:85], off offset:256
	v_add_f32_e32 v80, v80, v160
	v_add_f32_e32 v81, v81, v161
	v_add_f32_e32 v78, v78, v158
	v_add_f32_e32 v79, v79, v159
	v_add_u32_e32 v82, s35, v166
	v_mad_i64_i32 v[82:83], s[58:59], v82, s29, 0
	v_add_f32_e32 v76, v76, v156
	v_add_f32_e32 v77, v77, v157
	v_add_f32_e32 v74, v74, v154
	v_add_f32_e32 v75, v75, v155
	v_lshl_add_u64 v[82:83], v[82:83], 1, s[12:13]
	v_mul_f32_e32 v80, s28, v80
	v_mul_f32_e32 v81, s28, v81
	v_mul_f32_e32 v78, s28, v78
	v_mul_f32_e32 v79, s28, v79
	v_mul_f32_e32 v76, s28, v76
	v_mul_f32_e32 v77, s28, v77
	v_mul_f32_e32 v84, s28, v74
	v_mul_f32_e32 v85, s28, v75
	v_lshl_add_u64 v[82:83], v[82:83], 0, v[170:171]
	v_cvt_pk_f16_f32 v77, v76, v77
	v_cvt_pk_f16_f32 v75, v80, v81
	v_cvt_pk_f16_f32 v76, v84, v85
	v_cvt_pk_f16_f32 v74, v78, v79
	v_add_f32_e32 v72, v72, v152
	v_add_f32_e32 v73, v73, v153
	v_add_f32_e32 v70, v70, v150
	v_add_f32_e32 v71, v71, v151
	v_add_f32_e32 v68, v68, v148
	v_add_f32_e32 v69, v69, v149
	v_add_f32_e32 v66, v66, v146
	v_add_f32_e32 v67, v67, v147
	global_store_dwordx4 v[82:83], v[74:77], off
	v_mul_f32_e32 v72, s28, v72
	v_mul_f32_e32 v73, s28, v73
	v_mul_f32_e32 v70, s28, v70
	v_mul_f32_e32 v71, s28, v71
	v_mul_f32_e32 v68, s28, v68
	v_mul_f32_e32 v69, s28, v69
	v_mul_f32_e32 v74, s28, v66
	v_mul_f32_e32 v75, s28, v67
	s_add_i32 s35, s34, 0x90
	v_cvt_pk_f16_f32 v69, v68, v69
	v_cvt_pk_f16_f32 v67, v72, v73
	v_cvt_pk_f16_f32 v68, v74, v75
	v_cvt_pk_f16_f32 v66, v70, v71
	s_ashr_i32 s35, s35, 4
	global_store_dwordx4 v[82:83], v[66:69], off offset:256
	v_add_f32_e32 v64, v64, v160
	v_add_f32_e32 v65, v65, v161
	v_add_f32_e32 v62, v62, v158
	v_add_f32_e32 v63, v63, v159
	v_add_u32_e32 v66, s35, v166
	v_mad_i64_i32 v[66:67], s[58:59], v66, s29, 0
	v_add_f32_e32 v60, v60, v156
	v_add_f32_e32 v61, v61, v157
	v_add_f32_e32 v58, v58, v154
	v_add_f32_e32 v59, v59, v155
	v_lshl_add_u64 v[66:67], v[66:67], 1, s[12:13]
	v_mul_f32_e32 v64, s28, v64
	v_mul_f32_e32 v65, s28, v65
	v_mul_f32_e32 v62, s28, v62
	v_mul_f32_e32 v63, s28, v63
	v_mul_f32_e32 v60, s28, v60
	v_mul_f32_e32 v61, s28, v61
	v_mul_f32_e32 v68, s28, v58
	v_mul_f32_e32 v69, s28, v59
	v_lshl_add_u64 v[66:67], v[66:67], 0, v[170:171]
	v_cvt_pk_f16_f32 v61, v60, v61
	v_cvt_pk_f16_f32 v59, v64, v65
	v_cvt_pk_f16_f32 v60, v68, v69
	v_cvt_pk_f16_f32 v58, v62, v63
	v_add_f32_e32 v56, v56, v152
	v_add_f32_e32 v57, v57, v153
	v_add_f32_e32 v54, v54, v150
	v_add_f32_e32 v55, v55, v151
	v_add_f32_e32 v52, v52, v148
	v_add_f32_e32 v53, v53, v149
	v_add_f32_e32 v50, v50, v146
	v_add_f32_e32 v51, v51, v147
	global_store_dwordx4 v[66:67], v[58:61], off
	v_mul_f32_e32 v56, s28, v56
	v_mul_f32_e32 v57, s28, v57
	v_mul_f32_e32 v54, s28, v54
	v_mul_f32_e32 v55, s28, v55
	v_mul_f32_e32 v52, s28, v52
	v_mul_f32_e32 v53, s28, v53
	v_mul_f32_e32 v58, s28, v50
	v_mul_f32_e32 v59, s28, v51
	s_add_i32 s35, s34, 0xa0
	v_cvt_pk_f16_f32 v53, v52, v53
	v_cvt_pk_f16_f32 v51, v56, v57
	v_cvt_pk_f16_f32 v52, v58, v59
	v_cvt_pk_f16_f32 v50, v54, v55
	s_ashr_i32 s35, s35, 4
	global_store_dwordx4 v[66:67], v[50:53], off offset:256
	v_add_f32_e32 v48, v48, v160
	v_add_f32_e32 v49, v49, v161
	v_add_f32_e32 v46, v46, v158
	v_add_f32_e32 v47, v47, v159
	v_add_u32_e32 v50, s35, v166
	v_mad_i64_i32 v[50:51], s[58:59], v50, s29, 0
	v_add_f32_e32 v44, v44, v156
	v_add_f32_e32 v45, v45, v157
	v_add_f32_e32 v42, v42, v154
	v_add_f32_e32 v43, v43, v155
	v_lshl_add_u64 v[50:51], v[50:51], 1, s[12:13]
	v_mul_f32_e32 v48, s28, v48
	v_mul_f32_e32 v49, s28, v49
	v_mul_f32_e32 v46, s28, v46
	v_mul_f32_e32 v47, s28, v47
	v_mul_f32_e32 v44, s28, v44
	v_mul_f32_e32 v45, s28, v45
	v_mul_f32_e32 v52, s28, v42
	v_mul_f32_e32 v53, s28, v43
	v_lshl_add_u64 v[50:51], v[50:51], 0, v[170:171]
	v_cvt_pk_f16_f32 v45, v44, v45
	v_cvt_pk_f16_f32 v43, v48, v49
	v_cvt_pk_f16_f32 v44, v52, v53
	v_cvt_pk_f16_f32 v42, v46, v47
	v_add_f32_e32 v40, v40, v152
	v_add_f32_e32 v41, v41, v153
	v_add_f32_e32 v38, v38, v150
	v_add_f32_e32 v39, v39, v151
	v_add_f32_e32 v36, v36, v148
	v_add_f32_e32 v37, v37, v149
	v_add_f32_e32 v34, v34, v146
	v_add_f32_e32 v35, v35, v147
	global_store_dwordx4 v[50:51], v[42:45], off
	v_mul_f32_e32 v40, s28, v40
	v_mul_f32_e32 v41, s28, v41
	v_mul_f32_e32 v38, s28, v38
	v_mul_f32_e32 v39, s28, v39
	v_mul_f32_e32 v36, s28, v36
	v_mul_f32_e32 v37, s28, v37
	v_mul_f32_e32 v42, s28, v34
	v_mul_f32_e32 v43, s28, v35
	s_addk_i32 s34, 0xb0
	v_cvt_pk_f16_f32 v37, v36, v37
	v_cvt_pk_f16_f32 v35, v40, v41
	v_cvt_pk_f16_f32 v36, v42, v43
	v_cvt_pk_f16_f32 v34, v38, v39
	s_ashr_i32 s34, s34, 4
	global_store_dwordx4 v[50:51], v[34:37], off offset:256
	v_add_f32_e32 v32, v32, v160
	v_add_f32_e32 v33, v33, v161
	v_add_f32_e32 v30, v30, v158
	v_add_f32_e32 v31, v31, v159
	v_add_u32_e32 v34, s34, v166
	v_mad_i64_i32 v[34:35], s[34:35], v34, s29, 0
	v_add_f32_e32 v28, v28, v156
	v_add_f32_e32 v29, v29, v157
	v_add_f32_e32 v26, v26, v154
	v_add_f32_e32 v27, v27, v155
	v_lshl_add_u64 v[34:35], v[34:35], 1, s[12:13]
	v_mul_f32_e32 v32, s28, v32
	v_mul_f32_e32 v33, s28, v33
	v_mul_f32_e32 v30, s28, v30
	v_mul_f32_e32 v31, s28, v31
	v_mul_f32_e32 v28, s28, v28
	v_mul_f32_e32 v29, s28, v29
	v_mul_f32_e32 v36, s28, v26
	v_mul_f32_e32 v37, s28, v27
	v_lshl_add_u64 v[34:35], v[34:35], 0, v[170:171]
	v_cvt_pk_f16_f32 v29, v28, v29
	v_cvt_pk_f16_f32 v27, v32, v33
	v_cvt_pk_f16_f32 v28, v36, v37
	v_cvt_pk_f16_f32 v26, v30, v31
	v_add_f32_e32 v24, v24, v152
	v_add_f32_e32 v25, v25, v153
	v_add_f32_e32 v22, v22, v150
	v_add_f32_e32 v23, v23, v151
	v_add_f32_e32 v20, v20, v148
	v_add_f32_e32 v21, v21, v149
	v_add_f32_e32 v18, v18, v146
	v_add_f32_e32 v19, v19, v147
	global_store_dwordx4 v[34:35], v[26:29], off
	v_mul_f32_e32 v24, s28, v24
	v_mul_f32_e32 v25, s28, v25
	v_mul_f32_e32 v22, s28, v22
	v_mul_f32_e32 v23, s28, v23
	v_mul_f32_e32 v20, s28, v20
	v_mul_f32_e32 v21, s28, v21
	v_mul_f32_e32 v26, s28, v18
	v_mul_f32_e32 v27, s28, v19
	v_cvt_pk_f16_f32 v21, v20, v21
	v_cvt_pk_f16_f32 v19, v24, v25
	v_cvt_pk_f16_f32 v20, v26, v27
	v_cvt_pk_f16_f32 v18, v22, v23
	global_store_dwordx4 v[34:35], v[18:21], off offset:256
	s_cbranch_vccnz .LBB8_22
	s_mov_b32 s58, s36
	s_mov_b32 s57, s37
	s_mov_b64 s[34:35], s[30:31]
	s_branch .LBB8_8

.LBB8_45:
	v_lshl_or_b32 v166, s58, 8, v172
	v_ashrrev_i32_e32 v167, 31, v166
	s_waitcnt lgkmcnt(0)
	v_lshl_add_u64 v[144:145], v[166:167], 2, s[6:7]
	global_load_dwordx4 v[156:159], v[144:145], off
	global_load_dwordx4 v[152:155], v[144:145], off offset:16
	global_load_dwordx4 v[148:151], v[144:145], off offset:512
	s_nop 0
	global_load_dwordx4 v[144:147], v[144:145], off offset:528
	v_lshl_add_u32 v180, s57, 8, v176
	v_mad_i64_i32 v[182:183], s[24:25], v180, s47, 0
	v_or_b32_e32 v181, 16, v180
	v_lshl_add_u64 v[182:183], v[182:183], 1, s[4:5]
	v_lshlrev_b64 v[166:167], 1, v[166:167]
	v_mad_i64_i32 v[184:185], s[24:25], v181, s47, 0
	v_or_b32_e32 v186, 32, v180
	v_lshl_add_u64 v[182:183], v[182:183], 0, v[166:167]
	v_lshl_add_u64 v[184:185], v[184:185], 1, s[4:5]
	v_lshl_add_u64 v[184:185], v[184:185], 0, v[166:167]
	s_mov_b64 vcc, s[0:1]
	s_waitcnt vmcnt(0)
	v_add_f32_e32 v138, v138, v158
	v_add_f32_e32 v139, v139, v159
	v_add_f32_e32 v136, v136, v156
	v_add_f32_e32 v137, v137, v157
	v_add_f32_e32 v142, v142, v154
	v_add_f32_e32 v143, v143, v155
	v_add_f32_e32 v140, v140, v152
	v_add_f32_e32 v141, v141, v153
	v_add_f32_e32 v134, v134, v150
	v_add_f32_e32 v135, v135, v151
	v_add_f32_e32 v132, v132, v148
	v_add_f32_e32 v133, v133, v149
	v_add_f32_e32 v130, v130, v146
	v_add_f32_e32 v131, v131, v147
	v_add_f32_e32 v128, v128, v144
	v_add_f32_e32 v129, v129, v145
	v_add_f32_e32 v126, v126, v158
	v_add_f32_e32 v127, v127, v159
	v_add_f32_e32 v124, v124, v156
	v_add_f32_e32 v125, v125, v157
	v_add_f32_e32 v122, v122, v154
	v_add_f32_e32 v123, v123, v155
	v_add_f32_e32 v120, v120, v152
	v_add_f32_e32 v121, v121, v153
	v_add_f32_e32 v118, v118, v150
	v_add_f32_e32 v119, v119, v151
	v_add_f32_e32 v116, v116, v148
	v_add_f32_e32 v117, v117, v149
	v_add_f32_e32 v114, v114, v146
	v_add_f32_e32 v115, v115, v147
	v_add_f32_e32 v112, v112, v144
	v_add_f32_e32 v113, v113, v145
	v_max_f32_e32 v136, 0, v136
	v_max_f32_e32 v140, 0, v140
	v_max_f32_e32 v137, 0, v137
	v_max_f32_e32 v141, 0, v141
	v_max_f32_e32 v138, 0, v138
	v_max_f32_e32 v142, 0, v142
	v_max_f32_e32 v139, 0, v139
	v_max_f32_e32 v143, 0, v143
	v_max_f32_e32 v132, 0, v132
	v_max_f32_e32 v128, 0, v128
	v_max_f32_e32 v133, 0, v133
	v_max_f32_e32 v129, 0, v129
	v_max_f32_e32 v134, 0, v134
	v_max_f32_e32 v130, 0, v130
	v_max_f32_e32 v135, 0, v135
	v_max_f32_e32 v131, 0, v131
	v_max_f32_e32 v124, 0, v124
	v_max_f32_e32 v120, 0, v120
	v_max_f32_e32 v125, 0, v125
	v_max_f32_e32 v181, 0, v121
	v_max_f32_e32 v121, 0, v126
	v_max_f32_e32 v122, 0, v122
	v_max_f32_e32 v126, 0, v127
	v_max_f32_e32 v123, 0, v123
	v_max_f32_e32 v187, 0, v116
	v_max_f32_e32 v188, 0, v112
	v_max_f32_e32 v189, 0, v117
	v_max_f32_e32 v190, 0, v113
	v_max_f32_e32 v191, 0, v118
	v_max_f32_e32 v127, 0, v114
	v_max_f32_e32 v192, 0, v119
	v_max_f32_e32 v193, 0, v115
	v_cvt_pk_f16_f32 v115, v142, v143
	v_cvt_pk_f16_f32 v113, v138, v139
	v_cvt_pk_f16_f32 v114, v140, v141
	v_cvt_pk_f16_f32 v112, v136, v137
	v_cvt_pk_f16_f32 v119, v130, v131
	v_cvt_pk_f16_f32 v117, v134, v135
	v_cvt_pk_f16_f32 v118, v128, v129
	v_cvt_pk_f16_f32 v116, v132, v133
	v_cvt_pk_f16_f32 v123, v122, v123
	v_cvt_pk_f16_f32 v121, v121, v126
	v_cvt_pk_f16_f32 v122, v120, v181
	v_cvt_pk_f16_f32 v120, v124, v125
	v_cvt_pk_f16_f32 v127, v127, v193
	v_cvt_pk_f16_f32 v125, v191, v192
	v_cvt_pk_f16_f32 v126, v188, v190
	v_cvt_pk_f16_f32 v124, v187, v189
	global_store_dwordx4 v[182:183], v[112:115], off
	global_store_dwordx4 v[182:183], v[116:119], off offset:256
	global_store_dwordx4 v[184:185], v[120:123], off
	global_store_dwordx4 v[184:185], v[124:127], off offset:256
	v_mad_i64_i32 v[112:113], s[24:25], v186, s47, 0
	v_add_f32_e32 v110, v110, v158
	v_add_f32_e32 v111, v111, v159
	v_add_f32_e32 v108, v108, v156
	v_add_f32_e32 v109, v109, v157
	v_add_f32_e32 v106, v106, v154
	v_add_f32_e32 v107, v107, v155
	v_add_f32_e32 v104, v104, v152
	v_add_f32_e32 v105, v105, v153
	v_lshl_add_u64 v[112:113], v[112:113], 1, s[4:5]
	v_max_f32_e32 v108, 0, v108
	v_max_f32_e32 v104, 0, v104
	v_max_f32_e32 v109, 0, v109
	v_max_f32_e32 v114, 0, v105
	v_max_f32_e32 v105, 0, v110
	v_max_f32_e32 v106, 0, v106
	v_max_f32_e32 v110, 0, v111
	v_max_f32_e32 v107, 0, v107
	v_lshl_add_u64 v[112:113], v[112:113], 0, v[166:167]
	v_cvt_pk_f16_f32 v107, v106, v107
	v_cvt_pk_f16_f32 v105, v105, v110
	v_cvt_pk_f16_f32 v106, v104, v114
	v_cvt_pk_f16_f32 v104, v108, v109
	v_add_f32_e32 v102, v102, v150
	v_add_f32_e32 v103, v103, v151
	v_add_f32_e32 v100, v100, v148
	v_add_f32_e32 v101, v101, v149
	v_add_f32_e32 v98, v98, v146
	v_add_f32_e32 v99, v99, v147
	v_add_f32_e32 v96, v96, v144
	v_add_f32_e32 v97, v97, v145
	global_store_dwordx4 v[112:113], v[104:107], off
	v_max_f32_e32 v100, 0, v100
	v_max_f32_e32 v96, 0, v96
	v_max_f32_e32 v101, 0, v101
	v_max_f32_e32 v104, 0, v97
	v_max_f32_e32 v97, 0, v102
	v_max_f32_e32 v98, 0, v98
	v_max_f32_e32 v102, 0, v103
	v_max_f32_e32 v99, 0, v99
	v_cvt_pk_f16_f32 v99, v98, v99
	v_cvt_pk_f16_f32 v97, v97, v102
	v_cvt_pk_f16_f32 v98, v96, v104
	v_cvt_pk_f16_f32 v96, v100, v101
	global_store_dwordx4 v[112:113], v[96:99], off offset:256
	v_add_f32_e32 v94, v94, v158
	v_add_f32_e32 v95, v95, v159
	v_add_f32_e32 v92, v92, v156
	v_add_f32_e32 v93, v93, v157
	v_or_b32_e32 v96, 48, v180
	v_mad_i64_i32 v[96:97], s[24:25], v96, s47, 0
	v_add_f32_e32 v90, v90, v154
	v_add_f32_e32 v91, v91, v155
	v_add_f32_e32 v88, v88, v152
	v_add_f32_e32 v89, v89, v153
	v_lshl_add_u64 v[96:97], v[96:97], 1, s[4:5]
	v_max_f32_e32 v92, 0, v92
	v_max_f32_e32 v88, 0, v88
	v_max_f32_e32 v93, 0, v93
	v_max_f32_e32 v98, 0, v89
	v_max_f32_e32 v89, 0, v94
	v_max_f32_e32 v90, 0, v90
	v_max_f32_e32 v94, 0, v95
	v_max_f32_e32 v91, 0, v91
	v_lshl_add_u64 v[96:97], v[96:97], 0, v[166:167]
	v_cvt_pk_f16_f32 v91, v90, v91
	v_cvt_pk_f16_f32 v89, v89, v94
	v_cvt_pk_f16_f32 v90, v88, v98
	v_cvt_pk_f16_f32 v88, v92, v93
	v_add_f32_e32 v86, v86, v150
	v_add_f32_e32 v87, v87, v151
	v_add_f32_e32 v84, v84, v148
	v_add_f32_e32 v85, v85, v149
	v_add_f32_e32 v82, v82, v146
	v_add_f32_e32 v83, v83, v147
	v_add_f32_e32 v80, v80, v144
	v_add_f32_e32 v81, v81, v145
	global_store_dwordx4 v[96:97], v[88:91], off
	v_max_f32_e32 v84, 0, v84
	v_max_f32_e32 v80, 0, v80
	v_max_f32_e32 v85, 0, v85
	v_max_f32_e32 v88, 0, v81
	v_max_f32_e32 v81, 0, v86
	v_max_f32_e32 v82, 0, v82
	v_max_f32_e32 v86, 0, v87
	v_max_f32_e32 v83, 0, v83
	v_cvt_pk_f16_f32 v83, v82, v83
	v_cvt_pk_f16_f32 v81, v81, v86
	v_cvt_pk_f16_f32 v82, v80, v88
	v_cvt_pk_f16_f32 v80, v84, v85
	global_store_dwordx4 v[96:97], v[80:83], off offset:256
	v_add_f32_e32 v78, v78, v158
	v_add_f32_e32 v79, v79, v159
	v_add_f32_e32 v76, v76, v156
	v_add_f32_e32 v77, v77, v157
	v_add_u32_e32 v80, 0x80, v180
	v_mad_i64_i32 v[80:81], s[24:25], v80, s47, 0
	v_add_f32_e32 v74, v74, v154
	v_add_f32_e32 v75, v75, v155
	v_add_f32_e32 v72, v72, v152
	v_add_f32_e32 v73, v73, v153
	v_lshl_add_u64 v[80:81], v[80:81], 1, s[4:5]
	v_max_f32_e32 v76, 0, v76
	v_max_f32_e32 v72, 0, v72
	v_max_f32_e32 v77, 0, v77
	v_max_f32_e32 v82, 0, v73
	v_max_f32_e32 v73, 0, v78
	v_max_f32_e32 v74, 0, v74
	v_max_f32_e32 v78, 0, v79
	v_max_f32_e32 v75, 0, v75
	v_lshl_add_u64 v[80:81], v[80:81], 0, v[166:167]
	v_cvt_pk_f16_f32 v75, v74, v75
	v_cvt_pk_f16_f32 v73, v73, v78
	v_cvt_pk_f16_f32 v74, v72, v82
	v_cvt_pk_f16_f32 v72, v76, v77
	v_add_f32_e32 v70, v70, v150
	v_add_f32_e32 v71, v71, v151
	v_add_f32_e32 v68, v68, v148
	v_add_f32_e32 v69, v69, v149
	v_add_f32_e32 v66, v66, v146
	v_add_f32_e32 v67, v67, v147
	v_add_f32_e32 v64, v64, v144
	v_add_f32_e32 v65, v65, v145
	global_store_dwordx4 v[80:81], v[72:75], off
	v_max_f32_e32 v68, 0, v68
	v_max_f32_e32 v64, 0, v64
	v_max_f32_e32 v69, 0, v69
	v_max_f32_e32 v72, 0, v65
	v_max_f32_e32 v65, 0, v70
	v_max_f32_e32 v66, 0, v66
	v_max_f32_e32 v70, 0, v71
	v_max_f32_e32 v67, 0, v67
	v_cvt_pk_f16_f32 v67, v66, v67
	v_cvt_pk_f16_f32 v65, v65, v70
	v_cvt_pk_f16_f32 v66, v64, v72
	v_cvt_pk_f16_f32 v64, v68, v69
	global_store_dwordx4 v[80:81], v[64:67], off offset:256
	v_add_f32_e32 v62, v62, v158
	v_add_f32_e32 v63, v63, v159
	v_add_f32_e32 v60, v60, v156
	v_add_f32_e32 v61, v61, v157
	v_add_u32_e32 v64, 0x90, v180
	v_mad_i64_i32 v[64:65], s[24:25], v64, s47, 0
	v_add_f32_e32 v58, v58, v154
	v_add_f32_e32 v59, v59, v155
	v_add_f32_e32 v56, v56, v152
	v_add_f32_e32 v57, v57, v153
	v_lshl_add_u64 v[64:65], v[64:65], 1, s[4:5]
	v_max_f32_e32 v60, 0, v60
	v_max_f32_e32 v56, 0, v56
	v_max_f32_e32 v61, 0, v61
	v_max_f32_e32 v66, 0, v57
	v_max_f32_e32 v57, 0, v62
	v_max_f32_e32 v58, 0, v58
	v_max_f32_e32 v62, 0, v63
	v_max_f32_e32 v59, 0, v59
	v_lshl_add_u64 v[64:65], v[64:65], 0, v[166:167]
	v_cvt_pk_f16_f32 v59, v58, v59
	v_cvt_pk_f16_f32 v57, v57, v62
	v_cvt_pk_f16_f32 v58, v56, v66
	v_cvt_pk_f16_f32 v56, v60, v61
	v_add_f32_e32 v54, v54, v150
	v_add_f32_e32 v55, v55, v151
	v_add_f32_e32 v52, v52, v148
	v_add_f32_e32 v53, v53, v149
	v_add_f32_e32 v50, v50, v146
	v_add_f32_e32 v51, v51, v147
	v_add_f32_e32 v48, v48, v144
	v_add_f32_e32 v49, v49, v145
	global_store_dwordx4 v[64:65], v[56:59], off
	v_max_f32_e32 v52, 0, v52
	v_max_f32_e32 v48, 0, v48
	v_max_f32_e32 v53, 0, v53
	v_max_f32_e32 v56, 0, v49
	v_max_f32_e32 v49, 0, v54
	v_max_f32_e32 v50, 0, v50
	v_max_f32_e32 v54, 0, v55
	v_max_f32_e32 v51, 0, v51
	v_cvt_pk_f16_f32 v51, v50, v51
	v_cvt_pk_f16_f32 v49, v49, v54
	v_cvt_pk_f16_f32 v50, v48, v56
	v_cvt_pk_f16_f32 v48, v52, v53
	global_store_dwordx4 v[64:65], v[48:51], off offset:256
	v_add_f32_e32 v46, v46, v158
	v_add_f32_e32 v47, v47, v159
	v_add_f32_e32 v44, v44, v156
	v_add_f32_e32 v45, v45, v157
	v_add_u32_e32 v48, 0xa0, v180
	v_mad_i64_i32 v[48:49], s[24:25], v48, s47, 0
	v_add_f32_e32 v42, v42, v154
	v_add_f32_e32 v43, v43, v155
	v_add_f32_e32 v40, v40, v152
	v_add_f32_e32 v41, v41, v153
	v_lshl_add_u64 v[48:49], v[48:49], 1, s[4:5]
	v_max_f32_e32 v44, 0, v44
	v_max_f32_e32 v40, 0, v40
	v_max_f32_e32 v45, 0, v45
	v_max_f32_e32 v50, 0, v41
	v_max_f32_e32 v41, 0, v46
	v_max_f32_e32 v42, 0, v42
	v_max_f32_e32 v46, 0, v47
	v_max_f32_e32 v43, 0, v43
	v_lshl_add_u64 v[48:49], v[48:49], 0, v[166:167]
	v_cvt_pk_f16_f32 v43, v42, v43
	v_cvt_pk_f16_f32 v41, v41, v46
	v_cvt_pk_f16_f32 v42, v40, v50
	v_cvt_pk_f16_f32 v40, v44, v45
	v_add_f32_e32 v38, v38, v150
	v_add_f32_e32 v39, v39, v151
	v_add_f32_e32 v36, v36, v148
	v_add_f32_e32 v37, v37, v149
	v_add_f32_e32 v34, v34, v146
	v_add_f32_e32 v35, v35, v147
	v_add_f32_e32 v32, v32, v144
	v_add_f32_e32 v33, v33, v145
	global_store_dwordx4 v[48:49], v[40:43], off
	v_max_f32_e32 v36, 0, v36
	v_max_f32_e32 v32, 0, v32
	v_max_f32_e32 v37, 0, v37
	v_max_f32_e32 v40, 0, v33
	v_max_f32_e32 v33, 0, v38
	v_max_f32_e32 v34, 0, v34
	v_max_f32_e32 v38, 0, v39
	v_max_f32_e32 v35, 0, v35
	v_cvt_pk_f16_f32 v35, v34, v35
	v_cvt_pk_f16_f32 v33, v33, v38
	v_cvt_pk_f16_f32 v34, v32, v40
	v_cvt_pk_f16_f32 v32, v36, v37
	global_store_dwordx4 v[48:49], v[32:35], off offset:256
	v_add_f32_e32 v30, v30, v158
	v_add_f32_e32 v31, v31, v159
	v_add_f32_e32 v28, v28, v156
	v_add_f32_e32 v29, v29, v157
	v_add_u32_e32 v32, 0xb0, v180
	v_mad_i64_i32 v[32:33], s[24:25], v32, s47, 0
	v_add_f32_e32 v26, v26, v154
	v_add_f32_e32 v27, v27, v155
	v_add_f32_e32 v24, v24, v152
	v_add_f32_e32 v25, v25, v153
	v_lshl_add_u64 v[32:33], v[32:33], 1, s[4:5]
	v_max_f32_e32 v28, 0, v28
	v_max_f32_e32 v24, 0, v24
	v_max_f32_e32 v29, 0, v29
	v_max_f32_e32 v34, 0, v25
	v_max_f32_e32 v25, 0, v30
	v_max_f32_e32 v26, 0, v26
	v_max_f32_e32 v30, 0, v31
	v_max_f32_e32 v27, 0, v27
	v_lshl_add_u64 v[32:33], v[32:33], 0, v[166:167]
	v_cvt_pk_f16_f32 v27, v26, v27
	v_cvt_pk_f16_f32 v25, v25, v30
	v_cvt_pk_f16_f32 v26, v24, v34
	v_cvt_pk_f16_f32 v24, v28, v29
	v_add_f32_e32 v22, v22, v150
	v_add_f32_e32 v23, v23, v151
	v_add_f32_e32 v20, v20, v148
	v_add_f32_e32 v21, v21, v149
	v_add_f32_e32 v18, v18, v146
	v_add_f32_e32 v19, v19, v147
	v_add_f32_e32 v16, v16, v144
	v_add_f32_e32 v17, v17, v145
	global_store_dwordx4 v[32:33], v[24:27], off
	v_max_f32_e32 v20, 0, v20
	v_max_f32_e32 v16, 0, v16
	v_max_f32_e32 v21, 0, v21
	v_max_f32_e32 v24, 0, v17
	v_max_f32_e32 v17, 0, v22
	v_max_f32_e32 v18, 0, v18
	v_max_f32_e32 v22, 0, v23
	v_max_f32_e32 v19, 0, v19
	v_cvt_pk_f16_f32 v19, v18, v19
	v_cvt_pk_f16_f32 v17, v17, v22
	v_cvt_pk_f16_f32 v18, v16, v24
	v_cvt_pk_f16_f32 v16, v20, v21
	global_store_dwordx4 v[32:33], v[16:19], off offset:256
	s_cbranch_vccnz .LBB8_47
	s_mov_b32 s58, s55
	s_mov_b32 s57, s56
	s_mov_b64 s[24:25], s[22:23]
	s_branch .LBB8_33

.LBB9_11:
	v_lshlrev_b32_e32 v0, 2, v90
	v_lshl_or_b32 v0, s13, 5, v0
	v_or_b32_e32 v42, s12, v0
	v_ashrrev_i32_e32 v43, 31, v42
	s_waitcnt lgkmcnt(0)
	v_lshl_add_u64 v[44:45], v[42:43], 2, s[4:5]
	global_load_dwordx4 v[34:37], v[44:45], off
	global_load_dwordx4 v[38:41], v[44:45], off offset:64
	s_load_dword s4, s[0:1], 0x28
	s_lshl_b32 s0, s11, 6
	s_add_i32 s10, s10, s0
	v_or_b32_e32 v44, s10, v1
	v_or_b32_e32 v45, 16, v44
	v_or_b32_e32 v46, 32, v44
	v_or_b32_e32 v48, 48, v44
	v_lshl_add_u64 v[0:1], v[42:43], 1, s[2:3]
	s_waitcnt lgkmcnt(0)
	v_mad_i64_i32 v[42:43], s[0:1], v44, s4, 0
	v_mad_i64_i32 v[44:45], s[0:1], v45, s4, 0
	v_mad_i64_i32 v[46:47], s[0:1], v46, s4, 0
	v_mad_i64_i32 v[48:49], s[0:1], v48, s4, 0
	v_lshl_add_u64 v[42:43], v[42:43], 1, v[0:1]
	v_lshl_add_u64 v[44:45], v[44:45], 1, v[0:1]
	v_lshl_add_u64 v[46:47], v[46:47], 1, v[0:1]
	v_lshl_add_u64 v[0:1], v[48:49], 1, v[0:1]
	s_waitcnt vmcnt(0)
	v_add_f32_e32 v20, v36, v20
	v_add_f32_e32 v21, v37, v21
	v_add_f32_e32 v18, v34, v18
	v_add_f32_e32 v19, v35, v19
	v_add_f32_e32 v32, v36, v32
	v_add_f32_e32 v33, v37, v33
	v_add_f32_e32 v30, v34, v30
	v_add_f32_e32 v31, v35, v31
	v_add_f32_e32 v28, v36, v28
	v_add_f32_e32 v29, v37, v29
	v_add_f32_e32 v26, v34, v26
	v_add_f32_e32 v27, v35, v27
	v_add_f32_e32 v24, v36, v24
	v_add_f32_e32 v25, v37, v25
	v_add_f32_e32 v22, v34, v22
	v_add_f32_e32 v23, v35, v23
	v_add_f32_e32 v16, v40, v16
	v_add_f32_e32 v17, v41, v17
	v_add_f32_e32 v14, v38, v14
	v_add_f32_e32 v15, v39, v15
	v_add_f32_e32 v12, v40, v12
	v_add_f32_e32 v13, v41, v13
	v_add_f32_e32 v10, v38, v10
	v_add_f32_e32 v11, v39, v11
	v_add_f32_e32 v8, v40, v8
	v_add_f32_e32 v9, v41, v9
	v_add_f32_e32 v6, v38, v6
	v_add_f32_e32 v7, v39, v7
	v_max_f32_e32 v18, 0, v18
	v_max_f32_e32 v19, 0, v19
	v_max_f32_e32 v20, 0, v20
	v_max_f32_e32 v21, 0, v21
	v_max_f32_e32 v30, 0, v30
	v_max_f32_e32 v31, 0, v31
	v_max_f32_e32 v32, 0, v32
	v_max_f32_e32 v33, 0, v33
	v_max_f32_e32 v26, 0, v26
	v_max_f32_e32 v27, 0, v27
	v_max_f32_e32 v28, 0, v28
	v_max_f32_e32 v29, 0, v29
	v_max_f32_e32 v22, 0, v22
	v_max_f32_e32 v23, 0, v23
	v_max_f32_e32 v24, 0, v24
	v_max_f32_e32 v25, 0, v25
	v_max_f32_e32 v14, 0, v14
	v_max_f32_e32 v34, 0, v15
	v_max_f32_e32 v15, 0, v16
	v_max_f32_e32 v16, 0, v17
	v_max_f32_e32 v35, 0, v10
	v_max_f32_e32 v36, 0, v11
	v_max_f32_e32 v17, 0, v12
	v_max_f32_e32 v37, 0, v13
	v_max_f32_e32 v48, 0, v6
	v_max_f32_e32 v49, 0, v7
	v_max_f32_e32 v50, 0, v8
	v_max_f32_e32 v51, 0, v9
	v_cvt_pk_f16_f32 v7, v20, v21
	v_cvt_pk_f16_f32 v6, v18, v19
	v_add_f32_e32 v4, v40, v4
	v_add_f32_e32 v5, v41, v5
	v_add_f32_e32 v2, v38, v2
	v_add_f32_e32 v3, v39, v3
	v_cvt_pk_f16_f32 v9, v32, v33
	v_cvt_pk_f16_f32 v8, v30, v31
	v_cvt_pk_f16_f32 v11, v28, v29
	v_cvt_pk_f16_f32 v10, v26, v27
	v_cvt_pk_f16_f32 v13, v24, v25
	v_cvt_pk_f16_f32 v12, v22, v23
	v_cvt_pk_f16_f32 v15, v15, v16
	v_cvt_pk_f16_f32 v14, v14, v34
	v_cvt_pk_f16_f32 v17, v17, v37
	v_cvt_pk_f16_f32 v16, v35, v36
	v_cvt_pk_f16_f32 v19, v50, v51
	v_cvt_pk_f16_f32 v18, v48, v49
	global_store_dwordx2 v[42:43], v[6:7], off
	global_store_dwordx2 v[44:45], v[8:9], off
	global_store_dwordx2 v[46:47], v[10:11], off
	global_store_dwordx2 v[0:1], v[12:13], off
	global_store_dwordx2 v[42:43], v[14:15], off offset:32
	global_store_dwordx2 v[44:45], v[16:17], off offset:32
	global_store_dwordx2 v[46:47], v[18:19], off offset:32
	v_max_f32_e32 v2, 0, v2
	v_max_f32_e32 v6, 0, v3
	v_max_f32_e32 v3, 0, v4
	v_max_f32_e32 v4, 0, v5
	v_cvt_pk_f16_f32 v3, v3, v4
	v_cvt_pk_f16_f32 v2, v2, v6
	global_store_dwordx2 v[0:1], v[2:3], off offset:32
	s_endpgm
	.p2align	8

.LBB10_11:
	v_lshlrev_b32_e32 v0, 2, v56
	v_lshl_or_b32 v0, s13, 5, v0
	v_or_b32_e32 v26, s11, v0
	v_ashrrev_i32_e32 v27, 31, v26
	s_waitcnt lgkmcnt(0)
	v_lshl_add_u64 v[28:29], v[26:27], 2, s[4:5]
	global_load_dwordx4 v[18:21], v[28:29], off
	global_load_dwordx4 v[22:25], v[28:29], off offset:64
	s_load_dword s4, s[0:1], 0x28
	s_lshl_b32 s0, s12, 5
	s_add_i32 s0, s0, s10
	v_or_b32_e32 v28, s0, v1
	v_or_b32_e32 v29, 16, v28
	v_lshl_add_u64 v[0:1], v[26:27], 1, s[2:3]
	s_waitcnt lgkmcnt(0)
	v_mad_i64_i32 v[26:27], s[0:1], v28, s4, 0
	v_mad_i64_i32 v[28:29], s[0:1], v29, s4, 0
	v_lshl_add_u64 v[26:27], v[26:27], 1, v[0:1]
	v_lshl_add_u64 v[0:1], v[28:29], 1, v[0:1]
	s_waitcnt vmcnt(0)
	v_add_f32_e32 v12, v20, v12
	v_add_f32_e32 v13, v21, v13
	v_add_f32_e32 v10, v18, v10
	v_add_f32_e32 v11, v19, v11
	v_add_f32_e32 v16, v20, v16
	v_add_f32_e32 v17, v21, v17
	v_add_f32_e32 v14, v18, v14
	v_add_f32_e32 v15, v19, v15
	v_add_f32_e32 v8, v24, v8
	v_add_f32_e32 v9, v25, v9
	v_add_f32_e32 v6, v22, v6
	v_add_f32_e32 v7, v23, v7
	v_add_f32_e32 v4, v24, v4
	v_add_f32_e32 v5, v25, v5
	v_add_f32_e32 v2, v22, v2
	v_add_f32_e32 v3, v23, v3
	v_max_f32_e32 v10, 0, v10
	v_max_f32_e32 v11, 0, v11
	v_max_f32_e32 v12, 0, v12
	v_max_f32_e32 v13, 0, v13
	v_max_f32_e32 v14, 0, v14
	v_max_f32_e32 v15, 0, v15
	v_max_f32_e32 v16, 0, v16
	v_max_f32_e32 v17, 0, v17
	v_max_f32_e32 v6, 0, v6
	v_max_f32_e32 v18, 0, v7
	v_max_f32_e32 v7, 0, v8
	v_max_f32_e32 v8, 0, v9
	v_max_f32_e32 v19, 0, v2
	v_max_f32_e32 v20, 0, v3
	v_max_f32_e32 v9, 0, v4
	v_max_f32_e32 v21, 0, v5
	v_cvt_pk_f16_f32 v3, v12, v13
	v_cvt_pk_f16_f32 v2, v10, v11
	v_cvt_pk_f16_f32 v5, v16, v17
	v_cvt_pk_f16_f32 v4, v14, v15
	v_cvt_pk_f16_f32 v7, v7, v8
	v_cvt_pk_f16_f32 v6, v6, v18
	v_cvt_pk_f16_f32 v9, v9, v21
	v_cvt_pk_f16_f32 v8, v19, v20
	global_store_dwordx2 v[26:27], v[2:3], off
	global_store_dwordx2 v[0:1], v[4:5], off
	global_store_dwordx2 v[26:27], v[6:7], off offset:32
	global_store_dwordx2 v[0:1], v[8:9], off offset:32
	s_endpgm
	.p2align	8

.LBB11_11:
	v_lshlrev_b32_e32 v16, 2, v56
	v_lshl_or_b32 v16, s13, 5, v16
	v_or_b32_e32 v34, s11, v16
	v_ashrrev_i32_e32 v35, 31, v34
	s_waitcnt lgkmcnt(0)
	v_lshl_add_u64 v[20:21], v[34:35], 2, s[4:5]
	global_load_dwordx4 v[16:19], v[20:21], off
	v_mbcnt_lo_u32_b32 v22, -1, 0
	v_mbcnt_hi_u32_b32 v22, -1, v22
	v_and_b32_e32 v24, 64, v22
	v_xor_b32_e32 v23, 1, v22
	v_add_u32_e32 v24, 64, v24
	v_xor_b32_e32 v25, 2, v22
	v_cmp_lt_i32_e32 vcc, v23, v24
	v_xor_b32_e32 v26, 4, v22
	s_load_dword s4, s[0:1], 0x28
	v_cndmask_b32_e32 v23, v22, v23, vcc
	v_cmp_lt_i32_e32 vcc, v25, v24
	s_lshl_b32 s0, s12, 5
	s_add_i32 s0, s0, s10
	v_cndmask_b32_e32 v25, v22, v25, vcc
	v_cmp_lt_i32_e32 vcc, v26, v24
	s_waitcnt vmcnt(0)
	v_add_f32_e32 v14, v18, v14
	v_add_f32_e32 v15, v19, v15
	v_add_f32_e32 v12, v16, v12
	v_add_f32_e32 v13, v17, v13
	v_cndmask_b32_e32 v24, v22, v26, vcc
	v_lshlrev_b32_e32 v22, 2, v23
	v_max_f32_e32 v12, 0, v12
	v_max_f32_e32 v13, 0, v13
	v_max_f32_e32 v23, 0, v14
	v_max_f32_e32 v15, 0, v15
	ds_bpermute_b32 v26, v22, v12
	ds_bpermute_b32 v27, v22, v13
	ds_bpermute_b32 v28, v22, v23
	ds_bpermute_b32 v29, v22, v15
	v_lshlrev_b32_e32 v14, 2, v25
	s_waitcnt lgkmcnt(0)
	v_max_f32_e32 v25, v26, v26
	v_max_f32_e32 v26, v27, v27
	v_max_f32_e32 v27, v28, v28
	v_max_f32_e32 v28, v29, v29
	v_max_f32_e32 v12, v12, v25
	v_max_f32_e32 v13, v13, v26
	v_max_f32_e32 v23, v23, v27
	v_max_f32_e32 v28, v15, v28
	ds_bpermute_b32 v25, v14, v12
	ds_bpermute_b32 v26, v14, v13
	ds_bpermute_b32 v27, v14, v23
	ds_bpermute_b32 v29, v14, v28
	v_lshlrev_b32_e32 v15, 2, v24
	s_waitcnt lgkmcnt(3)
	v_max_f32_e32 v24, v25, v25
	s_waitcnt lgkmcnt(2)
	v_max_f32_e32 v25, v26, v26
	s_waitcnt lgkmcnt(1)
	v_max_f32_e32 v30, v27, v27
	s_waitcnt lgkmcnt(0)
	v_max_f32_e32 v29, v29, v29
	v_max_f32_e32 v27, v12, v24
	v_max_f32_e32 v26, v13, v25
	v_max_f32_e32 v25, v23, v30
	v_max_f32_e32 v31, v28, v29
	ds_bpermute_b32 v30, v15, v27
	ds_bpermute_b32 v29, v15, v26
	ds_bpermute_b32 v28, v15, v25
	ds_bpermute_b32 v32, v15, v31
	v_or_b32_e32 v24, s0, v55
	v_cmp_eq_u32_e32 vcc, 0, v54
	v_lshl_add_u64 v[12:13], v[34:35], 1, s[2:3]
	v_ashrrev_i32_e32 v23, 3, v24
	s_and_saveexec_b64 s[0:1], vcc
	s_cbranch_execz .LBB11_13
	s_waitcnt lgkmcnt(3)
	v_max_f32_e32 v30, v30, v30
	v_max_f32_e32 v27, v27, v27
	v_max_f32_e32 v30, v27, v30
	s_waitcnt lgkmcnt(2)
	v_max_f32_e32 v27, v29, v29
	v_max_f32_e32 v26, v26, v26
	s_waitcnt lgkmcnt(0)
	v_max_f32_e32 v32, v32, v32
	v_max_f32_e32 v31, v31, v31
	v_max_f32_e32 v26, v26, v27
	v_max_f32_e32 v27, v28, v28
	v_max_f32_e32 v25, v25, v25
	v_max_f32_e32 v31, v31, v32
	v_max_f32_e32 v25, v25, v27
	v_mad_i64_i32 v[28:29], s[2:3], v23, s4, 0
	v_cvt_pk_f16_f32 v27, v25, v31
	v_cvt_pk_f16_f32 v26, v30, v26
	v_lshl_add_u64 v[28:29], v[28:29], 1, v[12:13]
	global_store_dwordx2 v[28:29], v[26:27], off
.LBB11_13:
	s_or_b64 exec, exec, s[0:1]
	v_add_f32_e32 v8, v16, v8
	v_add_f32_e32 v9, v17, v9
	v_add_f32_e32 v10, v18, v10
	v_add_f32_e32 v11, v19, v11
	v_max_f32_e32 v8, 0, v8
	v_max_f32_e32 v9, 0, v9
	ds_bpermute_b32 v16, v22, v8
	ds_bpermute_b32 v17, v22, v9
	v_max_f32_e32 v18, 0, v10
	ds_bpermute_b32 v19, v22, v18
	v_max_f32_e32 v11, 0, v11
	s_waitcnt lgkmcnt(2)
	v_max_f32_e32 v10, v16, v16
	s_waitcnt lgkmcnt(1)
	v_max_f32_e32 v16, v17, v17
	v_max_f32_e32 v8, v8, v10
	v_max_f32_e32 v16, v9, v16
	ds_bpermute_b32 v10, v14, v8
	ds_bpermute_b32 v17, v14, v16
	s_waitcnt lgkmcnt(1)
	v_max_f32_e32 v9, v10, v10
	s_waitcnt lgkmcnt(0)
	v_max_f32_e32 v10, v17, v17
	ds_bpermute_b32 v17, v22, v11
	v_max_f32_e32 v10, v16, v10
	v_max_f32_e32 v16, v19, v19
	v_max_f32_e32 v16, v18, v16
	ds_bpermute_b32 v18, v14, v16
	s_waitcnt lgkmcnt(1)
	v_max_f32_e32 v17, v17, v17
	v_max_f32_e32 v19, v11, v17
	ds_bpermute_b32 v25, v14, v19
	v_max_f32_e32 v8, v8, v9
	s_waitcnt lgkmcnt(1)
	v_max_f32_e32 v11, v18, v18
	v_max_f32_e32 v11, v16, v11
	ds_bpermute_b32 v9, v15, v8
	s_waitcnt lgkmcnt(1)
	v_max_f32_e32 v16, v25, v25
	v_max_f32_e32 v19, v19, v16
	ds_bpermute_b32 v17, v15, v10
	ds_bpermute_b32 v18, v15, v11
	ds_bpermute_b32 v25, v15, v19
	v_or_b32_e32 v16, 16, v24
	v_ashrrev_i32_e32 v16, 3, v16
	s_and_saveexec_b64 s[0:1], vcc
	s_cbranch_execz .LBB11_15
	s_waitcnt lgkmcnt(3)
	v_max_f32_e32 v9, v9, v9
	v_max_f32_e32 v8, v8, v8
	v_max_f32_e32 v8, v8, v9
	s_waitcnt lgkmcnt(2)
	v_max_f32_e32 v9, v17, v17
	v_max_f32_e32 v10, v10, v10
	s_waitcnt lgkmcnt(0)
	v_max_f32_e32 v24, v25, v25
	v_max_f32_e32 v19, v19, v19
	v_max_f32_e32 v10, v10, v9
	v_max_f32_e32 v9, v18, v18
	v_max_f32_e32 v11, v11, v11
	v_max_f32_e32 v19, v19, v24
	v_max_f32_e32 v9, v11, v9
	v_cvt_pk_f16_f32 v8, v8, v10
	v_mad_i64_i32 v[10:11], s[2:3], v16, s4, 0
	v_cvt_pk_f16_f32 v9, v9, v19
	v_lshl_add_u64 v[10:11], v[10:11], 1, v[12:13]
	global_store_dwordx2 v[10:11], v[8:9], off
.LBB11_15:
	s_or_b64 exec, exec, s[0:1]
	s_waitcnt lgkmcnt(3)
	global_load_dwordx4 v[8:11], v[20:21], off offset:64
	s_waitcnt vmcnt(0)
	v_add_f32_e32 v6, v10, v6
	v_add_f32_e32 v7, v11, v7
	v_add_f32_e32 v4, v8, v4
	v_add_f32_e32 v5, v9, v5
	v_max_f32_e32 v6, 0, v6
	v_max_f32_e32 v4, 0, v4
	v_max_f32_e32 v5, 0, v5
	v_max_f32_e32 v7, 0, v7
	s_waitcnt lgkmcnt(2)
	ds_bpermute_b32 v17, v22, v4
	s_waitcnt lgkmcnt(2)
	ds_bpermute_b32 v18, v22, v5
	ds_bpermute_b32 v19, v22, v6
	ds_bpermute_b32 v20, v22, v7
	s_waitcnt lgkmcnt(3)
	v_max_f32_e32 v17, v17, v17
	s_waitcnt lgkmcnt(2)
	v_max_f32_e32 v18, v18, v18
	s_waitcnt lgkmcnt(1)
	v_max_f32_e32 v19, v19, v19
	s_waitcnt lgkmcnt(0)
	v_max_f32_e32 v20, v20, v20
	v_max_f32_e32 v4, v4, v17
	v_max_f32_e32 v5, v5, v18
	v_max_f32_e32 v17, v6, v19
	v_max_f32_e32 v7, v7, v20
	ds_bpermute_b32 v6, v14, v4
	ds_bpermute_b32 v18, v14, v5
	ds_bpermute_b32 v19, v14, v17
	ds_bpermute_b32 v20, v14, v7
	s_waitcnt lgkmcnt(3)
	v_max_f32_e32 v6, v6, v6
	s_waitcnt lgkmcnt(2)
	v_max_f32_e32 v18, v18, v18
	s_waitcnt lgkmcnt(1)
	v_max_f32_e32 v19, v19, v19
	s_waitcnt lgkmcnt(0)
	v_max_f32_e32 v20, v20, v20
	v_max_f32_e32 v6, v4, v6
	v_max_f32_e32 v5, v5, v18
	v_max_f32_e32 v4, v17, v19
	v_max_f32_e32 v19, v7, v20
	ds_bpermute_b32 v18, v15, v6
	ds_bpermute_b32 v17, v15, v5
	ds_bpermute_b32 v7, v15, v4
	ds_bpermute_b32 v20, v15, v19
	s_and_saveexec_b64 s[0:1], vcc
	s_cbranch_execz .LBB11_17
	s_waitcnt lgkmcnt(2)
	v_max_f32_e32 v17, v17, v17
	v_max_f32_e32 v5, v5, v5
	s_waitcnt lgkmcnt(0)
	v_max_f32_e32 v20, v20, v20
	v_max_f32_e32 v19, v19, v19
	v_max_f32_e32 v18, v18, v18
	v_max_f32_e32 v6, v6, v6
	v_max_f32_e32 v17, v5, v17
	v_max_f32_e32 v5, v7, v7
	v_max_f32_e32 v4, v4, v4
	v_max_f32_e32 v19, v19, v20
	v_max_f32_e32 v6, v6, v18
	v_max_f32_e32 v4, v4, v5
	v_cvt_pk_f16_f32 v5, v4, v19
	v_cvt_pk_f16_f32 v4, v6, v17
	v_mad_i64_i32 v[6:7], s[2:3], v23, s4, 0
	v_lshl_add_u64 v[6:7], v[6:7], 1, v[12:13]
	global_store_dwordx2 v[6:7], v[4:5], off offset:32
.LBB11_17:
	s_or_b64 exec, exec, s[0:1]
	v_add_f32_e32 v0, v8, v0
	v_add_f32_e32 v1, v9, v1
	v_add_f32_e32 v2, v10, v2
	v_add_f32_e32 v3, v11, v3
	v_max_f32_e32 v0, 0, v0
	v_max_f32_e32 v1, 0, v1
	ds_bpermute_b32 v4, v22, v0
	ds_bpermute_b32 v5, v22, v1
	v_max_f32_e32 v6, 0, v2
	s_waitcnt lgkmcnt(3)
	ds_bpermute_b32 v7, v22, v6
	v_max_f32_e32 v3, 0, v3
	s_waitcnt lgkmcnt(2)
	v_max_f32_e32 v2, v4, v4
	s_waitcnt lgkmcnt(1)
	v_max_f32_e32 v4, v5, v5
	v_max_f32_e32 v0, v0, v2
	v_max_f32_e32 v4, v1, v4
	ds_bpermute_b32 v2, v14, v0
	ds_bpermute_b32 v5, v14, v4
	s_waitcnt lgkmcnt(1)
	v_max_f32_e32 v1, v2, v2
	s_waitcnt lgkmcnt(0)
	v_max_f32_e32 v2, v5, v5
	ds_bpermute_b32 v5, v22, v3
	v_max_f32_e32 v2, v4, v2
	v_max_f32_e32 v4, v7, v7
	v_max_f32_e32 v6, v6, v4
	ds_bpermute_b32 v7, v14, v6
	s_waitcnt lgkmcnt(1)
	v_max_f32_e32 v4, v5, v5
	v_max_f32_e32 v8, v3, v4
	ds_bpermute_b32 v9, v14, v8
	v_max_f32_e32 v0, v0, v1
	s_waitcnt lgkmcnt(1)
	v_max_f32_e32 v3, v7, v7
	v_max_f32_e32 v3, v6, v3
	ds_bpermute_b32 v1, v15, v0
	s_waitcnt lgkmcnt(1)
	v_max_f32_e32 v6, v9, v9
	v_max_f32_e32 v6, v8, v6
	ds_bpermute_b32 v4, v15, v2
	ds_bpermute_b32 v5, v15, v3
	ds_bpermute_b32 v7, v15, v6
	s_and_saveexec_b64 s[0:1], vcc
	s_cbranch_execz .LBB11_19
	s_waitcnt lgkmcnt(3)
	v_max_f32_e32 v1, v1, v1
	v_max_f32_e32 v0, v0, v0
	v_max_f32_e32 v0, v0, v1
	s_waitcnt lgkmcnt(2)
	v_max_f32_e32 v1, v4, v4
	v_max_f32_e32 v2, v2, v2
	s_waitcnt lgkmcnt(0)
	v_max_f32_e32 v7, v7, v7
	v_max_f32_e32 v6, v6, v6
	v_max_f32_e32 v2, v2, v1
	v_max_f32_e32 v1, v5, v5
	v_max_f32_e32 v3, v3, v3
	v_max_f32_e32 v6, v6, v7
	v_max_f32_e32 v1, v3, v1
	v_cvt_pk_f16_f32 v0, v0, v2
	v_mad_i64_i32 v[2:3], s[0:1], v16, s4, 0
	v_cvt_pk_f16_f32 v1, v1, v6
	v_lshl_add_u64 v[2:3], v[2:3], 1, v[12:13]
	global_store_dwordx2 v[2:3], v[0:1], off offset:32

.LBB12_11:
	s_load_dwordx2 s[2:3], s[0:1], 0x20
	s_load_dwordx2 s[4:5], s[0:1], 0x30
	v_lshlrev_b32_e32 v0, 2, v56
	v_lshl_or_b32 v0, s9, 5, v0
	v_or_b32_e32 v18, s7, v0
	v_ashrrev_i32_e32 v19, 31, v18
	v_lshlrev_b64 v[26:27], 2, v[18:19]
	s_waitcnt lgkmcnt(0)
	v_lshl_add_u64 v[28:29], s[4:5], 0, v[26:27]
	global_load_dwordx4 v[18:21], v[28:29], off
	global_load_dwordx4 v[22:25], v[28:29], off offset:64
	s_load_dword s4, s[0:1], 0x28
	s_lshl_b32 s0, s8, 5
	s_add_i32 s0, s0, s6
	v_or_b32_e32 v28, s0, v1
	v_or_b32_e32 v29, 16, v28
	v_lshl_add_u64 v[0:1], s[2:3], 0, v[26:27]
	s_waitcnt lgkmcnt(0)
	v_mad_i64_i32 v[26:27], s[0:1], v28, s4, 0
	v_mad_i64_i32 v[28:29], s[0:1], v29, s4, 0
	v_lshl_add_u64 v[26:27], v[26:27], 2, v[0:1]
	v_lshl_add_u64 v[28:29], v[28:29], 2, v[0:1]
	s_waitcnt vmcnt(0)
	v_add_f32_e32 v12, v20, v12
	v_add_f32_e32 v13, v21, v13
	v_add_f32_e32 v0, v18, v10
	v_add_f32_e32 v1, v19, v11
	v_add_f32_e32 v10, v20, v16
	v_add_f32_e32 v11, v21, v17
	v_add_f32_e32 v14, v18, v14
	v_add_f32_e32 v15, v19, v15
	v_add_f32_e32 v16, v24, v8
	v_add_f32_e32 v17, v25, v9
	v_add_f32_e32 v8, v22, v6
	v_add_f32_e32 v9, v23, v7
	v_add_f32_e32 v18, v24, v4
	v_add_f32_e32 v19, v25, v5
	v_add_f32_e32 v20, v22, v2
	v_add_f32_e32 v21, v23, v3
	v_max_f32_e32 v0, 0, v0
	v_max_f32_e32 v1, 0, v1
	v_max_f32_e32 v2, 0, v12
	v_max_f32_e32 v3, 0, v13
	v_max_f32_e32 v4, 0, v14
	v_max_f32_e32 v5, 0, v15
	v_max_f32_e32 v6, 0, v10
	v_max_f32_e32 v7, 0, v11
	v_max_f32_e32 v8, 0, v8
	v_max_f32_e32 v9, 0, v9
	v_max_f32_e32 v10, 0, v16
	v_max_f32_e32 v11, 0, v17
	v_max_f32_e32 v12, 0, v20
	v_max_f32_e32 v13, 0, v21
	v_max_f32_e32 v14, 0, v18
	v_max_f32_e32 v15, 0, v19
	global_store_dwordx4 v[26:27], v[0:3], off
	global_store_dwordx4 v[28:29], v[4:7], off
	global_store_dwordx4 v[26:27], v[8:11], off offset:64
	global_store_dwordx4 v[28:29], v[12:15], off offset:64
	s_endpgm
	.p2align	8
